# v48 + weight-conversion pull loops: counted waits keep two items in flight per wave (other item's 16 loads counted, no store drain before the next item's loads)
# speedup vs baseline: 1.0011x; 1.0011x over previous
; __device__ __forceinline__ CvItem cv_item(Frame& F, int it) {
;     int r = it;
;     if (r < I_WIN0) return cv_make(F.in[7], DM, EIN, WSP(bf16, WS_WIN0), 0, r); r -= I_WIN0;
;     if (r < I_SQ) return cv_make(F.in[11], DM, DM, WSP(bf16, WS_WOUT0), 0, r); r -= I_SQ;
;     if (r < I_F) return cv_make(F.in[13], DM, DFF, WSP(bf16, WS_WGU0), 1, r, FFN8); r -= I_F;
;     if (r < I_F) return cv_make(F.in[14], DM, DFF, WSP(bf16, WS_WGU0), 2, r, FFN8); r -= I_F;
;     if (r < I_F) return cv_make(F.in[15], DFF, DM, WSP(bf16, WS_WD0), 0, r, FFN8); r -= I_F;
;     if (r < I_WIN1) return cv_make(F.in[19], DM, 2 * DM, WSP(bf16, WS_WIN1), 0, r); r -= I_WIN1;
;     if (r < I_SQ) return cv_make(F.in[27], DM, DM, WSP(bf16, WS_WOUT1), 0, r); r -= I_SQ;
;     if (r < 64 * I_G) { const int mtx = r >> 2, sub = r & 3, gt = mtx >> 5, zh = mtx & 31, z = zh >> 4, h = zh & 15;
;         return cv_make(F.in[gt ? 24 : 22] + (size_t)zh * 16384, 128, 128, WSP(bf16, WS_WGT) + (size_t)((z * 2 + gt) * 16 + h) * 16384, 0, sub); } r -= 64 * I_G;
;     const int w = r / (8 * I_ME), rr = r % (8 * I_ME), e = rr / I_ME, sub = rr % I_ME;
;     if (w == 0) return cv_make(F.in[31] + (size_t)e * DM * DFFE, DM, DFFE, (bf16*)(F.ws + WS_MWGU + (size_t)e * 2 * DFFE * DM), 1, sub, 1);
;     if (w == 1) return cv_make(F.in[32] + (size_t)e * DM * DFFE, DM, DFFE, (bf16*)(F.ws + WS_MWGU + (size_t)e * 2 * DFFE * DM), 2, sub, 1);
;     return cv_make(F.in[33] + (size_t)e * DFFE * DM, DFFE, DM, (bf16*)(F.ws + WS_MWD + (size_t)e * DM * DFFE), 0, sub, 1);
; __device__ __forceinline__ void moe_pull(Frame& F, int k, int until) {
;     ...
;         for (int t = 0; t < 8; t += 2) {
;             if (f + t + 1 < NQ) { mb = cv_item(F, NEARLY + f + t + 1); cv_load(mb, F.lane, vb); }
;             if (f + t < NQ) cv_finish(ma, F.lane, va, scr);
;             if (t + 2 < 8 && f + t + 2 < NQ) { ma = cv_item(F, NEARLY + f + t + 2); cv_load(ma, F.lane, va); }
;             if (f + t + 1 < NQ) cv_finish(mb, F.lane, vb, scr);
.LBB0_721:
	s_add_i32 s56, s45, s53
	s_cmp_lt_i32 s56, 0x15cff
	s_cselect_b64 s[16:17], -1, 0
	s_cmp_gt_i32 s56, 0x15cfe
	s_cbranch_scc0 .Lcv7_go0
	s_waitcnt vmcnt(0)
	s_branch .LBB0_746
.Lcv7_go0:
	s_add_i32 s6, s56, 0x2e00
	s_add_i32 s22, s56, 0x2e01
	s_cmpk_gt_i32 s6, 0x8fe
	s_mov_b64 s[20:21], -1
	s_cbranch_scc0 .LBB0_743
	s_cmpk_gt_u32 s6, 0x35fe
	s_cbranch_scc0 .LBB0_740
	s_cmpk_gt_u32 s6, 0x39fe
	s_cbranch_scc0 .LBB0_737
	s_cmpk_gt_u32 s6, 0x3afe
	s_cbranch_scc0 .LBB0_734
	s_lshr_b32 s2, s54, 12
	s_mul_hi_u32 s2, s2, 0x24924925
	s_mulk_i32 s2, 0x7000
	s_sub_i32 s2, s52, s2
	s_add_i32 s2, s53, s2
	s_bfe_u32 s6, s2, 0x70009
	s_mulk_i32 s6, 0x2493
	s_lshr_b32 s23, s6, 16
	s_mul_i32 s6, s23, 0xe00
	s_add_i32 s3, s56, 0xfffff301
	s_sub_i32 s6, s2, s6
	s_cmpk_gt_u32 s3, 0x6fff
	s_mul_i32 s46, s23, 0x3800000
	s_cbranch_scc0 .LBB0_731
	s_add_i32 s2, s56, 0xffff8301
	s_cmpk_gt_u32 s2, 0x6fff
	s_mov_b64 s[18:19], -1
	s_cbranch_scc0 .LBB0_729
	v_readlane_b32 s60, v250, 0
	v_readlane_b32 s62, v250, 2
	v_readlane_b32 s63, v250, 3
	s_add_u32 s2, s62, s46
	s_addc_u32 s3, s63, 0
	s_mul_i32 s12, s23, 0xe00000
	s_add_u32 s12, s25, s12
	s_addc_u32 s13, s26, 0
	s_lshl_b32 s19, s6, 5
	s_lshl_b32 s18, s6, 1
	s_and_b32 s19, s19, 0x7e0
	s_and_b32 s18, s18, 0x1f80
	s_mul_i32 s20, s19, 0x1c00
	s_add_u32 s12, s12, s20
	s_addc_u32 s13, s13, 0
	s_add_u32 s12, s12, s18
	s_addc_u32 s13, s13, 0
	s_lshl_b32 s18, s18, 13
	s_add_u32 s2, s2, s18
	s_addc_u32 s3, s3, 0
	s_lshl_b32 s18, s19, 2
	s_add_u32 s2, s2, s18
	v_readlane_b32 s61, v250, 1
	v_readlane_b32 s64, v250, 4
	v_readlane_b32 s65, v250, 5
	v_readlane_b32 s66, v250, 6
	v_readlane_b32 s67, v250, 7
	s_addc_u32 s3, s3, 0
	s_mov_b64 s[18:19], 0

; #define GAS __attribute__((address_space(1)))
; __device__ __forceinline__ void cv_load(const CvItem& m, int lane, f32x4 (&v)[16]) {
;     const int rr = lane >> 3, c4 = (lane & 7) * 4;
; #pragma unroll
;     for (int i = 0; i < 16; ++i) v[i] = __builtin_nontemporal_load((const GAS f32x4*)(m.src + (size_t)(8 * i + rr) * m.ldw + c4));
; }
.LBB0_745:
	v_mad_u64_u32 v[2:3], s[20:21], s18, v130, 0
	v_mad_u64_u32 v[10:11], s[20:21], s18, v138, 0
	v_mad_u64_u32 v[18:19], s[20:21], s18, v142, 0
	v_mad_u64_u32 v[26:27], s[20:21], s18, v146, 0
	v_mad_u64_u32 v[34:35], s[20:21], s18, v150, 0
	v_mad_u64_u32 v[42:43], s[20:21], s18, v154, 0
	v_mad_u64_u32 v[50:51], s[20:21], s18, v158, 0
	v_mad_u64_u32 v[58:59], s[20:21], s18, v162, 0
	v_mov_b32_e32 v4, v3
	v_mov_b32_e32 v12, v11
	v_mov_b32_e32 v20, v19
	v_mov_b32_e32 v28, v27
	v_mov_b32_e32 v36, v35
	v_mov_b32_e32 v44, v43
	v_mov_b32_e32 v52, v51
	v_mov_b32_e32 v60, v59
	v_mad_u64_u32 v[4:5], s[20:21], s19, v130, v[4:5]
	v_mad_u64_u32 v[12:13], s[20:21], s19, v138, v[12:13]
	v_mad_u64_u32 v[20:21], s[20:21], s19, v142, v[20:21]
	v_mad_u64_u32 v[28:29], s[20:21], s19, v146, v[28:29]
	v_mad_u64_u32 v[36:37], s[20:21], s19, v150, v[36:37]
	v_mad_u64_u32 v[44:45], s[20:21], s19, v154, v[44:45]
	v_mad_u64_u32 v[52:53], s[20:21], s19, v158, v[52:53]
	v_mad_u64_u32 v[60:61], s[20:21], s19, v162, v[60:61]
	v_mov_b32_e32 v3, v4
	v_mad_u64_u32 v[4:5], s[20:21], s18, v136, 0
	v_mov_b32_e32 v11, v12
	v_mad_u64_u32 v[12:13], s[20:21], s18, v140, 0
	v_mov_b32_e32 v19, v20
	v_mad_u64_u32 v[20:21], s[20:21], s18, v144, 0
	v_mov_b32_e32 v27, v28
	v_mad_u64_u32 v[28:29], s[20:21], s18, v148, 0
	v_mov_b32_e32 v35, v36
	v_mad_u64_u32 v[36:37], s[20:21], s18, v152, 0
	v_mov_b32_e32 v43, v44
	v_mad_u64_u32 v[44:45], s[20:21], s18, v156, 0
	v_mov_b32_e32 v51, v52
	v_mad_u64_u32 v[52:53], s[20:21], s18, v160, 0
	v_mov_b32_e32 v59, v60
	v_mad_u64_u32 v[60:61], s[20:21], s18, v164, 0
	v_mov_b32_e32 v6, v5
	v_mov_b32_e32 v14, v13
	v_mov_b32_e32 v22, v21
	v_mov_b32_e32 v30, v29
	v_mov_b32_e32 v38, v37
	v_mov_b32_e32 v46, v45
	v_mov_b32_e32 v54, v53
	v_mov_b32_e32 v62, v61
	v_mad_u64_u32 v[6:7], s[20:21], s19, v136, v[6:7]
	v_mad_u64_u32 v[14:15], s[20:21], s19, v140, v[14:15]
	v_mad_u64_u32 v[22:23], s[20:21], s19, v144, v[22:23]
	v_mad_u64_u32 v[30:31], s[20:21], s19, v148, v[30:31]
	v_mad_u64_u32 v[38:39], s[20:21], s19, v152, v[38:39]
	v_mad_u64_u32 v[46:47], s[20:21], s19, v156, v[46:47]
	v_mad_u64_u32 v[54:55], s[20:21], s19, v160, v[54:55]
	v_mad_u64_u32 v[62:63], s[18:19], s19, v164, v[62:63]
	v_mov_b32_e32 v5, v6
	v_mov_b32_e32 v13, v14
	v_mov_b32_e32 v21, v22
	v_mov_b32_e32 v29, v30
	v_mov_b32_e32 v37, v38
	v_mov_b32_e32 v45, v46
	v_mov_b32_e32 v53, v54
	v_mov_b32_e32 v61, v62
	v_lshl_add_u64 v[2:3], v[2:3], 2, s[2:3]
	v_lshlrev_b32_e32 v134, 2, v132
	v_lshl_add_u64 v[4:5], v[4:5], 2, s[2:3]
	v_lshl_add_u64 v[10:11], v[10:11], 2, s[2:3]
	v_lshl_add_u64 v[12:13], v[12:13], 2, s[2:3]
	v_lshl_add_u64 v[18:19], v[18:19], 2, s[2:3]
	v_lshl_add_u64 v[20:21], v[20:21], 2, s[2:3]
	v_lshl_add_u64 v[26:27], v[26:27], 2, s[2:3]
	v_lshl_add_u64 v[28:29], v[28:29], 2, s[2:3]
	v_lshl_add_u64 v[34:35], v[34:35], 2, s[2:3]
	v_lshl_add_u64 v[36:37], v[36:37], 2, s[2:3]
	v_lshl_add_u64 v[42:43], v[42:43], 2, s[2:3]
	v_lshl_add_u64 v[44:45], v[44:45], 2, s[2:3]
	v_lshl_add_u64 v[50:51], v[50:51], 2, s[2:3]
	v_lshl_add_u64 v[52:53], v[52:53], 2, s[2:3]
	v_lshl_add_u64 v[58:59], v[58:59], 2, s[2:3]
	v_lshl_add_u64 v[60:61], v[60:61], 2, s[2:3]
	v_lshl_add_u64 v[2:3], v[2:3], 0, v[134:135]
	v_lshl_add_u64 v[6:7], v[4:5], 0, v[134:135]
	v_lshl_add_u64 v[10:11], v[10:11], 0, v[134:135]
	v_lshl_add_u64 v[14:15], v[12:13], 0, v[134:135]
	v_lshl_add_u64 v[18:19], v[18:19], 0, v[134:135]
	v_lshl_add_u64 v[22:23], v[20:21], 0, v[134:135]
	v_lshl_add_u64 v[26:27], v[26:27], 0, v[134:135]
	v_lshl_add_u64 v[30:31], v[28:29], 0, v[134:135]
	v_lshl_add_u64 v[34:35], v[34:35], 0, v[134:135]
	v_lshl_add_u64 v[38:39], v[36:37], 0, v[134:135]
	v_lshl_add_u64 v[42:43], v[42:43], 0, v[134:135]
	v_lshl_add_u64 v[46:47], v[44:45], 0, v[134:135]
	v_lshl_add_u64 v[50:51], v[50:51], 0, v[134:135]
	v_lshl_add_u64 v[54:55], v[52:53], 0, v[134:135]
	v_lshl_add_u64 v[58:59], v[58:59], 0, v[134:135]
	v_lshl_add_u64 v[62:63], v[60:61], 0, v[134:135]
	global_load_dwordx4 v[2:5], v[2:3], off nt
	s_nop 0
	global_load_dwordx4 v[6:9], v[6:7], off nt
	s_nop 0
	global_load_dwordx4 v[10:13], v[10:11], off nt
	s_nop 0
	global_load_dwordx4 v[14:17], v[14:15], off nt
	s_nop 0
	global_load_dwordx4 v[18:21], v[18:19], off nt
	s_nop 0
	global_load_dwordx4 v[22:25], v[22:23], off nt
	s_nop 0
	global_load_dwordx4 v[26:29], v[26:27], off nt
	s_nop 0
	global_load_dwordx4 v[30:33], v[30:31], off nt
	s_nop 0
	global_load_dwordx4 v[34:37], v[34:35], off nt
	s_nop 0
	global_load_dwordx4 v[38:41], v[38:39], off nt
	s_nop 0
	global_load_dwordx4 v[42:45], v[42:43], off nt
	s_nop 0
	global_load_dwordx4 v[46:49], v[46:47], off nt
	s_nop 0
	global_load_dwordx4 v[50:53], v[50:51], off nt
	s_nop 0
	global_load_dwordx4 v[54:57], v[54:55], off nt
	s_nop 0
	global_load_dwordx4 v[58:61], v[58:59], off nt
	s_nop 0
	global_load_dwordx4 v[62:65], v[62:63], off nt
; #define GAS __attribute__((address_space(1)))
; #define LAS __attribute__((address_space(3)))
; #define LDS_WAIT() asm volatile("s_waitcnt lgkmcnt(0)" ::: "memory")
; __device__ __forceinline__ unsigned pk4_fp8(float a, float b, float c, float d) { int p = 0; p = __builtin_amdgcn_cvt_pk_fp8_f32(a, b, p, false); p = __builtin_amdgcn_cvt_pk_fp8_f32(c, d, p, true); return (unsigned)p; }
; __device__ __forceinline__ float clamp8s(float x) { return __builtin_amdgcn_fmed3f(x * W8_SCALE, -448.0f, 448.0f); }
; __device__ __forceinline__ void cv_finish(const CvItem& m, int lane, const f32x4 (&v)[16], LAS float* scr) {
;     const int rr = lane >> 3, c4 = (lane & 7) * 4;
; #pragma unroll
;     for (int i = 0; i < 16; ++i) *(LAS f32x4*)(scr + (8 * i + rr) * 36 + (c4 ^ (4 * ((i >> 1) & 7)))) = v[i];
;     LDS_WAIT(); asm volatile("" ::: "memory");
;     const int kc = lane & 7, nn = lane >> 3;
; #pragma unroll
;     for (int j = 0; j < 4; ++j) { const int n = nn + 8 * j; const LAS float* s = scr + (16 * kc) * 36 + (n ^ (4 * kc));
;         float x[16];
; #pragma unroll
;         for (int q = 0; q < 16; ++q) x[q] = s[q * 36];
;         if (m.f8) { v4u o;
;             o.x = pk4_fp8(clamp8s(x[0]), clamp8s(x[1]), clamp8s(x[2]), clamp8s(x[3])); o.y = pk4_fp8(clamp8s(x[4]), clamp8s(x[5]), clamp8s(x[6]), clamp8s(x[7]));
;             o.z = pk4_fp8(clamp8s(x[8]), clamp8s(x[9]), clamp8s(x[10]), clamp8s(x[11])); o.w = pk4_fp8(clamp8s(x[12]), clamp8s(x[13]), clamp8s(x[14]), clamp8s(x[15]));
;             __builtin_nontemporal_store(o, (GAS v4u*)((unsigned char*)m.dst + (size_t)n * m.ldt + 16 * kc)); }
.LBB0_746:
	s_cmp_gt_i32 s56, 0x15cff
	v_add_u32_e32 v161, 0x400, v151
	v_add_u32_e32 v163, 0x600, v151
	s_cbranch_scc1 .LBB0_760
	s_waitcnt vmcnt(31)
	ds_write_b128 v1, v[66:69]
	s_waitcnt vmcnt(30)
	ds_write_b128 v131, v[70:73]
	s_waitcnt vmcnt(29)
	ds_write_b128 v133, v[74:77]
	s_waitcnt vmcnt(28)
	ds_write_b128 v137, v[78:81]
	s_waitcnt vmcnt(27)
	ds_write_b128 v139, v[82:85] offset:4608
	s_waitcnt vmcnt(26)
	ds_write_b128 v139, v[86:89] offset:5760
	s_waitcnt vmcnt(25)
	ds_write_b128 v141, v[90:93] offset:6912
	s_waitcnt vmcnt(24)
	ds_write_b128 v141, v[94:97] offset:8064
	s_waitcnt vmcnt(23)
	ds_write_b128 v143, v[98:101] offset:9216
	s_waitcnt vmcnt(22)
	ds_write_b128 v143, v[102:105] offset:10368
	s_waitcnt vmcnt(21)
	ds_write_b128 v145, v[106:109] offset:11520
	s_waitcnt vmcnt(20)
	ds_write_b128 v145, v[110:113] offset:12672
	s_waitcnt vmcnt(19)
	ds_write_b128 v147, v[114:117] offset:13824
	s_waitcnt vmcnt(18)
	ds_write_b128 v147, v[118:121] offset:14976
	s_waitcnt vmcnt(17)
	ds_write_b128 v149, v[122:125] offset:16128
	s_waitcnt vmcnt(16)
	ds_write_b128 v149, v[126:129] offset:17280
	s_waitcnt lgkmcnt(0)
	ds_read2_b32 v[182:183], v151 offset1:36
	ds_read2_b32 v[180:181], v151 offset0:72 offset1:108
	ds_read2_b32 v[178:179], v151 offset0:144 offset1:180
	ds_read2_b32 v[176:177], v151 offset0:216 offset1:252
	ds_read2_b32 v[174:175], v161 offset0:32 offset1:68
	ds_read2_b32 v[172:173], v161 offset0:104 offset1:140
	ds_read2_b32 v[170:171], v161 offset0:176 offset1:212
	ds_read2_b32 v[168:169], v163 offset0:120 offset1:156
	s_cmp_lg_u32 s48, 0
	s_cselect_b64 s[18:19], -1, 0
	s_cmp_eq_u32 s48, 0
	s_cbranch_scc1 .LBB0_793
	s_waitcnt lgkmcnt(7)
	v_mul_f32_e32 v134, 0x42800000, v182
	v_mul_f32_e32 v165, 0x42800000, v183
	v_med3_f32 v134, v134, s43, v159
	v_med3_f32 v165, v165, s43, v159
	v_mov_b32_e32 v184, v135
	v_cvt_pk_fp8_f32 v184, v134, v165
	s_waitcnt lgkmcnt(6)
	v_mul_f32_e32 v185, 0x42800000, v180
	v_mul_f32_e32 v165, 0x42800000, v181
	v_med3_f32 v134, v185, s43, v159
	v_med3_f32 v165, v165, s43, v159
	v_cvt_pk_fp8_f32 v184, v134, v165 op_sel:[0,0,1]
	s_waitcnt lgkmcnt(5)
	v_mul_f32_e32 v134, 0x42800000, v178
	v_mul_f32_e32 v165, 0x42800000, v179
	v_med3_f32 v134, v134, s43, v159
	v_med3_f32 v165, v165, s43, v159
	v_mov_b32_e32 v185, v135
	v_cvt_pk_fp8_f32 v185, v134, v165
	s_waitcnt lgkmcnt(4)
	v_mul_f32_e32 v186, 0x42800000, v176
	v_mul_f32_e32 v165, 0x42800000, v177
	v_med3_f32 v134, v186, s43, v159
	v_med3_f32 v165, v165, s43, v159
	v_cvt_pk_fp8_f32 v185, v134, v165 op_sel:[0,0,1]
	s_waitcnt lgkmcnt(3)
	v_mul_f32_e32 v134, 0x42800000, v174
	v_mul_f32_e32 v165, 0x42800000, v175
	v_med3_f32 v134, v134, s43, v159
	v_med3_f32 v165, v165, s43, v159
	v_mov_b32_e32 v186, v135
	v_cvt_pk_fp8_f32 v186, v134, v165
	s_waitcnt lgkmcnt(2)
	v_mul_f32_e32 v187, 0x42800000, v172
	v_mul_f32_e32 v165, 0x42800000, v173
	v_med3_f32 v134, v187, s43, v159
	v_med3_f32 v165, v165, s43, v159
	v_cvt_pk_fp8_f32 v186, v134, v165 op_sel:[0,0,1]
	s_waitcnt lgkmcnt(1)
	v_mul_f32_e32 v134, 0x42800000, v170
	v_mul_f32_e32 v165, 0x42800000, v171
	v_med3_f32 v134, v134, s43, v159
	v_med3_f32 v165, v165, s43, v159
	v_mov_b32_e32 v187, v135
	v_cvt_pk_fp8_f32 v187, v134, v165
	s_waitcnt lgkmcnt(0)
	v_mul_f32_e32 v188, 0x42800000, v168
	v_mul_f32_e32 v165, 0x42800000, v169
	v_med3_f32 v134, v188, s43, v159
	v_med3_f32 v165, v165, s43, v159
	v_cvt_pk_fp8_f32 v187, v134, v165 op_sel:[0,0,1]
	v_mov_b64_e32 v[188:189], s[14:15]
	v_mad_i64_i32 v[188:189], s[2:3], s47, v130, v[188:189]
	v_lshl_add_u64 v[188:189], v[188:189], 0, v[166:167]
	global_store_dwordx4 v[188:189], v[184:187], off nt
	s_cbranch_execnz .LBB0_750

; __device__ __forceinline__ CvItem cv_item(Frame& F, int it) {
;     int r = it;
;     if (r < I_WIN0) return cv_make(F.in[7], DM, EIN, WSP(bf16, WS_WIN0), 0, r); r -= I_WIN0;
;     if (r < I_SQ) return cv_make(F.in[11], DM, DM, WSP(bf16, WS_WOUT0), 0, r); r -= I_SQ;
;     if (r < I_F) return cv_make(F.in[13], DM, DFF, WSP(bf16, WS_WGU0), 1, r, FFN8); r -= I_F;
;     if (r < I_F) return cv_make(F.in[14], DM, DFF, WSP(bf16, WS_WGU0), 2, r, FFN8); r -= I_F;
;     if (r < I_F) return cv_make(F.in[15], DFF, DM, WSP(bf16, WS_WD0), 0, r, FFN8); r -= I_F;
;     if (r < I_WIN1) return cv_make(F.in[19], DM, 2 * DM, WSP(bf16, WS_WIN1), 0, r); r -= I_WIN1;
;     if (r < I_SQ) return cv_make(F.in[27], DM, DM, WSP(bf16, WS_WOUT1), 0, r); r -= I_SQ;
;     if (r < 64 * I_G) { const int mtx = r >> 2, sub = r & 3, gt = mtx >> 5, zh = mtx & 31, z = zh >> 4, h = zh & 15;
;         return cv_make(F.in[gt ? 24 : 22] + (size_t)zh * 16384, 128, 128, WSP(bf16, WS_WGT) + (size_t)((z * 2 + gt) * 16 + h) * 16384, 0, sub); } r -= 64 * I_G;
;     const int w = r / (8 * I_ME), rr = r % (8 * I_ME), e = rr / I_ME, sub = rr % I_ME;
;     if (w == 0) return cv_make(F.in[31] + (size_t)e * DM * DFFE, DM, DFFE, (bf16*)(F.ws + WS_MWGU + (size_t)e * 2 * DFFE * DM), 1, sub, 1);
;     if (w == 1) return cv_make(F.in[32] + (size_t)e * DM * DFFE, DM, DFFE, (bf16*)(F.ws + WS_MWGU + (size_t)e * 2 * DFFE * DM), 2, sub, 1);
;     return cv_make(F.in[33] + (size_t)e * DFFE * DM, DFFE, DM, (bf16*)(F.ws + WS_MWD + (size_t)e * DM * DFFE), 0, sub, 1);
; __device__ __forceinline__ void moe_pull(Frame& F, int k, int until) {
;     ...
;         for (int t = 0; t < 8; t += 2) {
;             if (f + t + 1 < NQ) { mb = cv_item(F, NEARLY + f + t + 1); cv_load(mb, F.lane, vb); }
;             if (f + t < NQ) cv_finish(ma, F.lane, va, scr);
;             if (t + 2 < 8 && f + t + 2 < NQ) { ma = cv_item(F, NEARLY + f + t + 2); cv_load(ma, F.lane, va); }
;             if (f + t + 1 < NQ) cv_finish(mb, F.lane, vb, scr);
.LBB0_760:
	s_cmp_gt_u32 s53, 5
	s_cselect_b64 s[18:19], -1, 0
	s_cmp_gt_i32 s56, 0x15cfd
	s_cselect_b64 s[2:3], -1, 0
	s_or_b64 s[2:3], s[18:19], s[2:3]
	s_and_b64 vcc, exec, s[2:3]
	s_cbranch_vccz .Lcv7_go1
	s_waitcnt vmcnt(0)
	s_branch .LBB0_781
.Lcv7_go1:
	s_add_i32 s6, s56, 0x2e00
	s_cmpk_gt_u32 s6, 0x35fd
	s_mov_b64 s[22:23], -1
	s_cbranch_scc0 .LBB0_778
	s_cmpk_gt_u32 s6, 0x39fd
	s_cbranch_scc0 .LBB0_775
	s_cmpk_gt_u32 s6, 0x3afd
	s_cbranch_scc0 .LBB0_772
	s_lshr_b32 s2, s55, 12
	s_mul_hi_u32 s2, s2, 0x24924925
	s_mulk_i32 s2, 0x7000
	s_sub_i32 s2, s49, s2
	s_add_i32 s2, s53, s2
	s_bfe_u32 s6, s2, 0x70009
	s_mulk_i32 s6, 0x2493
	s_lshr_b32 s48, s6, 16
	s_mul_i32 s6, s48, 0xe00
	s_add_i32 s3, s56, 0xfffff302
	s_sub_i32 s6, s2, s6
	s_cmpk_gt_u32 s3, 0x6fff
	s_mul_i32 s57, s48, 0x3800000
	s_cbranch_scc0 .LBB0_769
	s_add_i32 s2, s56, 0xffff8302
	s_cmpk_gt_u32 s2, 0x6fff
	s_mov_b64 s[20:21], -1
	s_cbranch_scc0 .LBB0_767
	v_readlane_b32 s60, v250, 0
	v_readlane_b32 s62, v250, 2
	v_readlane_b32 s63, v250, 3
	s_add_u32 s2, s62, s57
	s_addc_u32 s3, s63, 0
	s_mul_i32 s14, s48, 0xe00000
	s_add_u32 s14, s25, s14
	s_addc_u32 s15, s26, 0
	s_lshl_b32 s21, s6, 5
	s_lshl_b32 s20, s6, 1
	s_and_b32 s21, s21, 0x7e0
	s_and_b32 s20, s20, 0x1f80
	s_mul_i32 s22, s21, 0x1c00
	s_add_u32 s14, s14, s22
	s_addc_u32 s15, s15, 0
	s_add_u32 s14, s14, s20
	s_addc_u32 s15, s15, 0
	s_lshl_b32 s20, s20, 13
	s_add_u32 s2, s2, s20
	s_addc_u32 s3, s3, 0
	s_lshl_b32 s20, s21, 2
	s_add_u32 s2, s2, s20
	v_readlane_b32 s61, v250, 1
	v_readlane_b32 s64, v250, 4
	v_readlane_b32 s65, v250, 5
	v_readlane_b32 s66, v250, 6
	v_readlane_b32 s67, v250, 7
	s_addc_u32 s3, s3, 0
	s_mov_b64 s[20:21], 0

; #define GAS __attribute__((address_space(1)))
; __device__ __forceinline__ void cv_load(const CvItem& m, int lane, f32x4 (&v)[16]) {
;     const int rr = lane >> 3, c4 = (lane & 7) * 4;
; #pragma unroll
;     for (int i = 0; i < 16; ++i) v[i] = __builtin_nontemporal_load((const GAS f32x4*)(m.src + (size_t)(8 * i + rr) * m.ldw + c4));
; }
.LBB0_780:
	v_mad_u64_u32 v[66:67], s[22:23], s20, v130, 0
	v_mad_u64_u32 v[74:75], s[22:23], s20, v138, 0
	v_mad_u64_u32 v[82:83], s[22:23], s20, v142, 0
	v_mad_u64_u32 v[90:91], s[22:23], s20, v146, 0
	v_mad_u64_u32 v[98:99], s[22:23], s20, v150, 0
	v_mad_u64_u32 v[106:107], s[22:23], s20, v154, 0
	v_mad_u64_u32 v[114:115], s[22:23], s20, v158, 0
	v_mad_u64_u32 v[122:123], s[22:23], s20, v162, 0
	v_mov_b32_e32 v68, v67
	v_mov_b32_e32 v76, v75
	v_mov_b32_e32 v84, v83
	v_mov_b32_e32 v92, v91
	v_mov_b32_e32 v100, v99
	v_mov_b32_e32 v108, v107
	v_mov_b32_e32 v116, v115
	v_mov_b32_e32 v124, v123
	v_mad_u64_u32 v[68:69], s[22:23], s21, v130, v[68:69]
	v_mad_u64_u32 v[76:77], s[22:23], s21, v138, v[76:77]
	v_mad_u64_u32 v[84:85], s[22:23], s21, v142, v[84:85]
	v_mad_u64_u32 v[92:93], s[22:23], s21, v146, v[92:93]
	v_mad_u64_u32 v[100:101], s[22:23], s21, v150, v[100:101]
	v_mad_u64_u32 v[108:109], s[22:23], s21, v154, v[108:109]
	v_mad_u64_u32 v[116:117], s[22:23], s21, v158, v[116:117]
	v_mad_u64_u32 v[124:125], s[22:23], s21, v162, v[124:125]
	v_mov_b32_e32 v67, v68
	v_mad_u64_u32 v[68:69], s[22:23], s20, v136, 0
	v_mov_b32_e32 v75, v76
	v_mad_u64_u32 v[76:77], s[22:23], s20, v140, 0
	v_mov_b32_e32 v83, v84
	v_mad_u64_u32 v[84:85], s[22:23], s20, v144, 0
	v_mov_b32_e32 v91, v92
	v_mad_u64_u32 v[92:93], s[22:23], s20, v148, 0
	v_mov_b32_e32 v99, v100
	v_mad_u64_u32 v[100:101], s[22:23], s20, v152, 0
	v_mov_b32_e32 v107, v108
	v_mad_u64_u32 v[108:109], s[22:23], s20, v156, 0
	v_mov_b32_e32 v115, v116
	v_mad_u64_u32 v[116:117], s[22:23], s20, v160, 0
	v_mov_b32_e32 v123, v124
	v_mad_u64_u32 v[124:125], s[22:23], s20, v164, 0
	v_mov_b32_e32 v70, v69
	v_mov_b32_e32 v78, v77
	v_mov_b32_e32 v86, v85
	v_mov_b32_e32 v94, v93
	v_mov_b32_e32 v102, v101
	v_mov_b32_e32 v110, v109
	v_mov_b32_e32 v118, v117
	v_mov_b32_e32 v126, v125
	v_mad_u64_u32 v[70:71], s[22:23], s21, v136, v[70:71]
	v_mad_u64_u32 v[78:79], s[22:23], s21, v140, v[78:79]
	v_mad_u64_u32 v[86:87], s[22:23], s21, v144, v[86:87]
	v_mad_u64_u32 v[94:95], s[22:23], s21, v148, v[94:95]
	v_mad_u64_u32 v[102:103], s[22:23], s21, v152, v[102:103]
	v_mad_u64_u32 v[110:111], s[22:23], s21, v156, v[110:111]
	v_mad_u64_u32 v[118:119], s[22:23], s21, v160, v[118:119]
	v_mad_u64_u32 v[126:127], s[20:21], s21, v164, v[126:127]
	v_mov_b32_e32 v69, v70
	v_mov_b32_e32 v77, v78
	v_mov_b32_e32 v85, v86
	v_mov_b32_e32 v93, v94
	v_mov_b32_e32 v101, v102
	v_mov_b32_e32 v109, v110
	v_mov_b32_e32 v117, v118
	v_mov_b32_e32 v125, v126
	v_lshl_add_u64 v[66:67], v[66:67], 2, s[2:3]
	v_lshlrev_b32_e32 v134, 2, v132
	v_lshl_add_u64 v[68:69], v[68:69], 2, s[2:3]
	v_lshl_add_u64 v[74:75], v[74:75], 2, s[2:3]
	v_lshl_add_u64 v[76:77], v[76:77], 2, s[2:3]
	v_lshl_add_u64 v[82:83], v[82:83], 2, s[2:3]
	v_lshl_add_u64 v[84:85], v[84:85], 2, s[2:3]
	v_lshl_add_u64 v[90:91], v[90:91], 2, s[2:3]
	v_lshl_add_u64 v[92:93], v[92:93], 2, s[2:3]
	v_lshl_add_u64 v[98:99], v[98:99], 2, s[2:3]
	v_lshl_add_u64 v[100:101], v[100:101], 2, s[2:3]
	v_lshl_add_u64 v[106:107], v[106:107], 2, s[2:3]
	v_lshl_add_u64 v[108:109], v[108:109], 2, s[2:3]
	v_lshl_add_u64 v[114:115], v[114:115], 2, s[2:3]
	v_lshl_add_u64 v[116:117], v[116:117], 2, s[2:3]
	v_lshl_add_u64 v[122:123], v[122:123], 2, s[2:3]
	v_lshl_add_u64 v[124:125], v[124:125], 2, s[2:3]
	v_lshl_add_u64 v[66:67], v[66:67], 0, v[134:135]
	v_lshl_add_u64 v[70:71], v[68:69], 0, v[134:135]
	v_lshl_add_u64 v[74:75], v[74:75], 0, v[134:135]
	v_lshl_add_u64 v[78:79], v[76:77], 0, v[134:135]
	v_lshl_add_u64 v[82:83], v[82:83], 0, v[134:135]
	v_lshl_add_u64 v[86:87], v[84:85], 0, v[134:135]
	v_lshl_add_u64 v[90:91], v[90:91], 0, v[134:135]
	v_lshl_add_u64 v[94:95], v[92:93], 0, v[134:135]
	v_lshl_add_u64 v[98:99], v[98:99], 0, v[134:135]
	v_lshl_add_u64 v[102:103], v[100:101], 0, v[134:135]
	v_lshl_add_u64 v[106:107], v[106:107], 0, v[134:135]
	v_lshl_add_u64 v[110:111], v[108:109], 0, v[134:135]
	v_lshl_add_u64 v[114:115], v[114:115], 0, v[134:135]
	v_lshl_add_u64 v[118:119], v[116:117], 0, v[134:135]
	v_lshl_add_u64 v[122:123], v[122:123], 0, v[134:135]
	v_lshl_add_u64 v[126:127], v[124:125], 0, v[134:135]
	global_load_dwordx4 v[66:69], v[66:67], off nt
	s_nop 0
	global_load_dwordx4 v[70:73], v[70:71], off nt
	s_nop 0
	global_load_dwordx4 v[74:77], v[74:75], off nt
	s_nop 0
	global_load_dwordx4 v[78:81], v[78:79], off nt
	s_nop 0
	global_load_dwordx4 v[82:85], v[82:83], off nt
	s_nop 0
	global_load_dwordx4 v[86:89], v[86:87], off nt
	s_nop 0
	global_load_dwordx4 v[90:93], v[90:91], off nt
	s_nop 0
	global_load_dwordx4 v[94:97], v[94:95], off nt
	s_nop 0
	global_load_dwordx4 v[98:101], v[98:99], off nt
	s_nop 0
	global_load_dwordx4 v[102:105], v[102:103], off nt
	s_nop 0
	global_load_dwordx4 v[106:109], v[106:107], off nt
	s_nop 0
	global_load_dwordx4 v[110:113], v[110:111], off nt
	s_nop 0
	global_load_dwordx4 v[114:117], v[114:115], off nt
	s_nop 0
	global_load_dwordx4 v[118:121], v[118:119], off nt
	s_nop 0
	global_load_dwordx4 v[122:125], v[122:123], off nt
	s_nop 0
	global_load_dwordx4 v[126:129], v[126:127], off nt
; #define GAS __attribute__((address_space(1)))
; #define LAS __attribute__((address_space(3)))
; #define LDS_WAIT() asm volatile("s_waitcnt lgkmcnt(0)" ::: "memory")
; __device__ __forceinline__ unsigned pk4_fp8(float a, float b, float c, float d) { int p = 0; p = __builtin_amdgcn_cvt_pk_fp8_f32(a, b, p, false); p = __builtin_amdgcn_cvt_pk_fp8_f32(c, d, p, true); return (unsigned)p; }
; __device__ __forceinline__ float clamp8s(float x) { return __builtin_amdgcn_fmed3f(x * W8_SCALE, -448.0f, 448.0f); }
; __device__ __forceinline__ void cv_finish(const CvItem& m, int lane, const f32x4 (&v)[16], LAS float* scr) {
;     const int rr = lane >> 3, c4 = (lane & 7) * 4;
; #pragma unroll
;     for (int i = 0; i < 16; ++i) *(LAS f32x4*)(scr + (8 * i + rr) * 36 + (c4 ^ (4 * ((i >> 1) & 7)))) = v[i];
;     LDS_WAIT(); asm volatile("" ::: "memory");
;     const int kc = lane & 7, nn = lane >> 3;
; #pragma unroll
;     for (int j = 0; j < 4; ++j) { const int n = nn + 8 * j; const LAS float* s = scr + (16 * kc) * 36 + (n ^ (4 * kc));
;         float x[16];
; #pragma unroll
;         for (int q = 0; q < 16; ++q) x[q] = s[q * 36];
;         if (m.f8) { v4u o;
;             o.x = pk4_fp8(clamp8s(x[0]), clamp8s(x[1]), clamp8s(x[2]), clamp8s(x[3])); o.y = pk4_fp8(clamp8s(x[4]), clamp8s(x[5]), clamp8s(x[6]), clamp8s(x[7]));
;             o.z = pk4_fp8(clamp8s(x[8]), clamp8s(x[9]), clamp8s(x[10]), clamp8s(x[11])); o.w = pk4_fp8(clamp8s(x[12]), clamp8s(x[13]), clamp8s(x[14]), clamp8s(x[15]));
;             __builtin_nontemporal_store(o, (GAS v4u*)((unsigned char*)m.dst + (size_t)n * m.ldt + 16 * kc)); }
.LBB0_781:
	s_andn2_b64 vcc, exec, s[16:17]
	s_cbranch_vccnz .LBB0_720
	s_waitcnt vmcnt(31)
	ds_write_b128 v1, v[2:5]
	s_waitcnt vmcnt(30)
	ds_write_b128 v131, v[6:9]
	s_waitcnt vmcnt(29)
	ds_write_b128 v133, v[10:13]
	s_waitcnt vmcnt(28)
	ds_write_b128 v137, v[14:17]
	s_waitcnt vmcnt(27)
	ds_write_b128 v139, v[18:21] offset:4608
	s_waitcnt vmcnt(26)
	ds_write_b128 v139, v[22:25] offset:5760
	s_waitcnt vmcnt(25)
	ds_write_b128 v141, v[26:29] offset:6912
	s_waitcnt vmcnt(24)
	ds_write_b128 v141, v[30:33] offset:8064
	s_waitcnt vmcnt(23)
	ds_write_b128 v143, v[34:37] offset:9216
	s_waitcnt vmcnt(22)
	ds_write_b128 v143, v[38:41] offset:10368
	s_waitcnt vmcnt(21)
	ds_write_b128 v145, v[42:45] offset:11520
	s_waitcnt vmcnt(20)
	ds_write_b128 v145, v[46:49] offset:12672
	s_waitcnt vmcnt(19)
	ds_write_b128 v147, v[50:53] offset:13824
	s_waitcnt vmcnt(18)
	ds_write_b128 v147, v[54:57] offset:14976
	s_waitcnt vmcnt(17)
	ds_write_b128 v149, v[58:61] offset:16128
	s_waitcnt vmcnt(16)
	ds_write_b128 v149, v[62:65] offset:17280
	s_waitcnt lgkmcnt(0)
	s_waitcnt lgkmcnt(14)
	ds_read2_b32 v[182:183], v151 offset1:36
	ds_read2_b32 v[180:181], v151 offset0:72 offset1:108
	ds_read2_b32 v[178:179], v151 offset0:144 offset1:180
	ds_read2_b32 v[176:177], v151 offset0:216 offset1:252
	ds_read2_b32 v[174:175], v161 offset0:32 offset1:68
	ds_read2_b32 v[172:173], v161 offset0:104 offset1:140
	ds_read2_b32 v[170:171], v161 offset0:176 offset1:212
	ds_read2_b32 v[168:169], v163 offset0:120 offset1:156
	s_cmp_lg_u32 s46, 0
	s_cselect_b64 s[16:17], -1, 0
	s_cmp_eq_u32 s46, 0
	s_cbranch_scc1 .LBB0_797
	s_waitcnt lgkmcnt(7)
	v_mul_f32_e32 v134, 0x42800000, v182
	v_mul_f32_e32 v161, 0x42800000, v183
	v_med3_f32 v134, v134, s43, v159
	v_med3_f32 v161, v161, s43, v159
	v_mov_b32_e32 v184, v135
	v_cvt_pk_fp8_f32 v184, v134, v161
	s_waitcnt lgkmcnt(6)
	v_mul_f32_e32 v163, 0x42800000, v180
	v_mul_f32_e32 v161, 0x42800000, v181
	v_med3_f32 v134, v163, s43, v159
	v_med3_f32 v161, v161, s43, v159
	v_cvt_pk_fp8_f32 v184, v134, v161 op_sel:[0,0,1]
	s_waitcnt lgkmcnt(5)
	v_mul_f32_e32 v134, 0x42800000, v178
	v_mul_f32_e32 v161, 0x42800000, v179
	v_med3_f32 v134, v134, s43, v159
	v_med3_f32 v161, v161, s43, v159
	v_mov_b32_e32 v185, v135
	v_cvt_pk_fp8_f32 v185, v134, v161
	s_waitcnt lgkmcnt(4)
	v_mul_f32_e32 v163, 0x42800000, v176
	v_mul_f32_e32 v161, 0x42800000, v177
	v_med3_f32 v134, v163, s43, v159
	v_med3_f32 v161, v161, s43, v159
	v_cvt_pk_fp8_f32 v185, v134, v161 op_sel:[0,0,1]
	s_waitcnt lgkmcnt(3)
	v_mul_f32_e32 v134, 0x42800000, v174
	v_mul_f32_e32 v161, 0x42800000, v175
	v_med3_f32 v134, v134, s43, v159
	v_med3_f32 v161, v161, s43, v159
	v_mov_b32_e32 v186, v135
	v_cvt_pk_fp8_f32 v186, v134, v161
	s_waitcnt lgkmcnt(2)
	v_mul_f32_e32 v163, 0x42800000, v172
	v_mul_f32_e32 v161, 0x42800000, v173
	v_med3_f32 v134, v163, s43, v159
	v_med3_f32 v161, v161, s43, v159
	v_cvt_pk_fp8_f32 v186, v134, v161 op_sel:[0,0,1]
	s_waitcnt lgkmcnt(1)
	v_mul_f32_e32 v134, 0x42800000, v170
	v_mul_f32_e32 v161, 0x42800000, v171
	v_med3_f32 v134, v134, s43, v159
	v_med3_f32 v161, v161, s43, v159
	v_mov_b32_e32 v187, v135
	v_cvt_pk_fp8_f32 v187, v134, v161
	s_waitcnt lgkmcnt(0)
	v_mul_f32_e32 v163, 0x42800000, v168
	v_mul_f32_e32 v161, 0x42800000, v169
	v_med3_f32 v134, v163, s43, v159
	v_med3_f32 v161, v161, s43, v159
	v_cvt_pk_fp8_f32 v187, v134, v161 op_sel:[0,0,1]
	v_mov_b64_e32 v[188:189], s[12:13]
	v_mad_i64_i32 v[188:189], s[2:3], s44, v130, v[188:189]
	v_lshl_add_u64 v[188:189], v[188:189], 0, v[166:167]
	global_store_dwordx4 v[188:189], v[184:187], off nt
	v_lshlrev_b32_e32 v134, 1, v166
	s_cbranch_execnz .LBB0_785

; __device__ __forceinline__ CvItem cv_item(Frame& F, int it) {
;     int r = it;
;     if (r < I_WIN0) return cv_make(F.in[7], DM, EIN, WSP(bf16, WS_WIN0), 0, r); r -= I_WIN0;
;     if (r < I_SQ) return cv_make(F.in[11], DM, DM, WSP(bf16, WS_WOUT0), 0, r); r -= I_SQ;
;     if (r < I_F) return cv_make(F.in[13], DM, DFF, WSP(bf16, WS_WGU0), 1, r, FFN8); r -= I_F;
;     if (r < I_F) return cv_make(F.in[14], DM, DFF, WSP(bf16, WS_WGU0), 2, r, FFN8); r -= I_F;
;     if (r < I_F) return cv_make(F.in[15], DFF, DM, WSP(bf16, WS_WD0), 0, r, FFN8); r -= I_F;
;     if (r < I_WIN1) return cv_make(F.in[19], DM, 2 * DM, WSP(bf16, WS_WIN1), 0, r); r -= I_WIN1;
;     if (r < I_SQ) return cv_make(F.in[27], DM, DM, WSP(bf16, WS_WOUT1), 0, r); r -= I_SQ;
;     if (r < 64 * I_G) { const int mtx = r >> 2, sub = r & 3, gt = mtx >> 5, zh = mtx & 31, z = zh >> 4, h = zh & 15;
;         return cv_make(F.in[gt ? 24 : 22] + (size_t)zh * 16384, 128, 128, WSP(bf16, WS_WGT) + (size_t)((z * 2 + gt) * 16 + h) * 16384, 0, sub); } r -= 64 * I_G;
;     const int w = r / (8 * I_ME), rr = r % (8 * I_ME), e = rr / I_ME, sub = rr % I_ME;
;     if (w == 0) return cv_make(F.in[31] + (size_t)e * DM * DFFE, DM, DFFE, (bf16*)(F.ws + WS_MWGU + (size_t)e * 2 * DFFE * DM), 1, sub, 1);
;     if (w == 1) return cv_make(F.in[32] + (size_t)e * DM * DFFE, DM, DFFE, (bf16*)(F.ws + WS_MWGU + (size_t)e * 2 * DFFE * DM), 2, sub, 1);
;     return cv_make(F.in[33] + (size_t)e * DFFE * DM, DFFE, DM, (bf16*)(F.ws + WS_MWD + (size_t)e * DM * DFFE), 0, sub, 1);
; __device__ __forceinline__ void moe_pull(Frame& F, int k, int until) {
;     ...
;         for (int t = 0; t < 8; t += 2) {
;             if (f + t + 1 < NQ) { mb = cv_item(F, NEARLY + f + t + 1); cv_load(mb, F.lane, vb); }
;             if (f + t < NQ) cv_finish(ma, F.lane, va, scr);
;             if (t + 2 < 8 && f + t + 2 < NQ) { ma = cv_item(F, NEARLY + f + t + 2); cv_load(ma, F.lane, va); }
;             if (f + t + 1 < NQ) cv_finish(mb, F.lane, vb, scr);
.LBB0_1103:
	s_add_i32 s54, s43, s51
	s_cmp_lt_i32 s54, 0x15cff
	s_cselect_b64 s[14:15], -1, 0
	s_cmp_gt_i32 s54, 0x15cfe
	s_cbranch_scc0 .Lcv9_go0
	s_waitcnt vmcnt(0)
	s_branch .LBB0_1128
.Lcv9_go0:
	s_add_i32 s6, s54, 0x2e00
	s_add_i32 s20, s54, 0x2e01
	s_cmpk_gt_i32 s6, 0x8fe
	s_mov_b64 s[18:19], -1
	s_cbranch_scc0 .LBB0_1125
	s_cmpk_gt_u32 s6, 0x35fe
	s_cbranch_scc0 .LBB0_1122
	s_cmpk_gt_u32 s6, 0x39fe
	s_cbranch_scc0 .LBB0_1119
	s_cmpk_gt_u32 s6, 0x3afe
	s_cbranch_scc0 .LBB0_1116
	s_lshr_b32 s2, s52, 12
	s_mul_hi_u32 s2, s2, 0x24924925
	s_mulk_i32 s2, 0x7000
	s_sub_i32 s2, s50, s2
	s_add_i32 s2, s51, s2
	s_bfe_u32 s6, s2, 0x70009
	s_mulk_i32 s6, 0x2493
	s_lshr_b32 s21, s6, 16
	s_mul_i32 s6, s21, 0xe00
	s_add_i32 s3, s54, 0xfffff301
	s_sub_i32 s6, s2, s6
	s_cmpk_gt_u32 s3, 0x6fff
	s_mul_i32 s44, s21, 0x3800000
	s_cbranch_scc0 .LBB0_1113
	s_add_i32 s2, s54, 0xffff8301
	s_cmpk_gt_u32 s2, 0x6fff
	s_mov_b64 s[16:17], -1
	s_cbranch_scc0 .LBB0_1111
	v_readlane_b32 s56, v250, 0
	v_readlane_b32 s58, v250, 2
	v_readlane_b32 s59, v250, 3
	s_add_u32 s2, s58, s44
	s_addc_u32 s3, s59, 0
	s_mul_i32 s10, s21, 0xe00000
	s_add_u32 s10, s23, s10
	s_addc_u32 s11, s24, 0
	s_lshl_b32 s17, s6, 5
	s_lshl_b32 s16, s6, 1
	s_and_b32 s17, s17, 0x7e0
	s_and_b32 s16, s16, 0x1f80
	s_mul_i32 s18, s17, 0x1c00
	s_add_u32 s10, s10, s18
	s_addc_u32 s11, s11, 0
	s_add_u32 s10, s10, s16
	s_addc_u32 s11, s11, 0
	s_lshl_b32 s16, s16, 13
	s_add_u32 s2, s2, s16
	s_addc_u32 s3, s3, 0
	s_lshl_b32 s16, s17, 2
	s_add_u32 s2, s2, s16
	v_readlane_b32 s57, v250, 1
	v_readlane_b32 s60, v250, 4
	v_readlane_b32 s61, v250, 5
	v_readlane_b32 s62, v250, 6
	v_readlane_b32 s63, v250, 7
	s_addc_u32 s3, s3, 0
	s_mov_b64 s[16:17], 0

; #define GAS __attribute__((address_space(1)))
; __device__ __forceinline__ void cv_load(const CvItem& m, int lane, f32x4 (&v)[16]) {
;     const int rr = lane >> 3, c4 = (lane & 7) * 4;
; #pragma unroll
;     for (int i = 0; i < 16; ++i) v[i] = __builtin_nontemporal_load((const GAS f32x4*)(m.src + (size_t)(8 * i + rr) * m.ldw + c4));
; }
.LBB0_1127:
	v_mad_u64_u32 v[2:3], s[18:19], s16, v130, 0
	v_mad_u64_u32 v[10:11], s[18:19], s16, v138, 0
	v_mad_u64_u32 v[18:19], s[18:19], s16, v142, 0
	v_mad_u64_u32 v[26:27], s[18:19], s16, v146, 0
	v_mad_u64_u32 v[34:35], s[18:19], s16, v150, 0
	v_mad_u64_u32 v[42:43], s[18:19], s16, v154, 0
	v_mad_u64_u32 v[50:51], s[18:19], s16, v158, 0
	v_mad_u64_u32 v[58:59], s[18:19], s16, v162, 0
	v_mov_b32_e32 v4, v3
	v_mov_b32_e32 v12, v11
	v_mov_b32_e32 v20, v19
	v_mov_b32_e32 v28, v27
	v_mov_b32_e32 v36, v35
	v_mov_b32_e32 v44, v43
	v_mov_b32_e32 v52, v51
	v_mov_b32_e32 v60, v59
	v_mad_u64_u32 v[4:5], s[18:19], s17, v130, v[4:5]
	v_mad_u64_u32 v[12:13], s[18:19], s17, v138, v[12:13]
	v_mad_u64_u32 v[20:21], s[18:19], s17, v142, v[20:21]
	v_mad_u64_u32 v[28:29], s[18:19], s17, v146, v[28:29]
	v_mad_u64_u32 v[36:37], s[18:19], s17, v150, v[36:37]
	v_mad_u64_u32 v[44:45], s[18:19], s17, v154, v[44:45]
	v_mad_u64_u32 v[52:53], s[18:19], s17, v158, v[52:53]
	v_mad_u64_u32 v[60:61], s[18:19], s17, v162, v[60:61]
	v_mov_b32_e32 v3, v4
	v_mad_u64_u32 v[4:5], s[18:19], s16, v136, 0
	v_mov_b32_e32 v11, v12
	v_mad_u64_u32 v[12:13], s[18:19], s16, v140, 0
	v_mov_b32_e32 v19, v20
	v_mad_u64_u32 v[20:21], s[18:19], s16, v144, 0
	v_mov_b32_e32 v27, v28
	v_mad_u64_u32 v[28:29], s[18:19], s16, v148, 0
	v_mov_b32_e32 v35, v36
	v_mad_u64_u32 v[36:37], s[18:19], s16, v152, 0
	v_mov_b32_e32 v43, v44
	v_mad_u64_u32 v[44:45], s[18:19], s16, v156, 0
	v_mov_b32_e32 v51, v52
	v_mad_u64_u32 v[52:53], s[18:19], s16, v160, 0
	v_mov_b32_e32 v59, v60
	v_mad_u64_u32 v[60:61], s[18:19], s16, v164, 0
	v_mov_b32_e32 v6, v5
	v_mov_b32_e32 v14, v13
	v_mov_b32_e32 v22, v21
	v_mov_b32_e32 v30, v29
	v_mov_b32_e32 v38, v37
	v_mov_b32_e32 v46, v45
	v_mov_b32_e32 v54, v53
	v_mov_b32_e32 v62, v61
	v_mad_u64_u32 v[6:7], s[18:19], s17, v136, v[6:7]
	v_mad_u64_u32 v[14:15], s[18:19], s17, v140, v[14:15]
	v_mad_u64_u32 v[22:23], s[18:19], s17, v144, v[22:23]
	v_mad_u64_u32 v[30:31], s[18:19], s17, v148, v[30:31]
	v_mad_u64_u32 v[38:39], s[18:19], s17, v152, v[38:39]
	v_mad_u64_u32 v[46:47], s[18:19], s17, v156, v[46:47]
	v_mad_u64_u32 v[54:55], s[18:19], s17, v160, v[54:55]
	v_mad_u64_u32 v[62:63], s[16:17], s17, v164, v[62:63]
	v_mov_b32_e32 v5, v6
	v_mov_b32_e32 v13, v14
	v_mov_b32_e32 v21, v22
	v_mov_b32_e32 v29, v30
	v_mov_b32_e32 v37, v38
	v_mov_b32_e32 v45, v46
	v_mov_b32_e32 v53, v54
	v_mov_b32_e32 v61, v62
	v_lshl_add_u64 v[2:3], v[2:3], 2, s[2:3]
	v_lshlrev_b32_e32 v134, 2, v132
	v_lshl_add_u64 v[4:5], v[4:5], 2, s[2:3]
	v_lshl_add_u64 v[10:11], v[10:11], 2, s[2:3]
	v_lshl_add_u64 v[12:13], v[12:13], 2, s[2:3]
	v_lshl_add_u64 v[18:19], v[18:19], 2, s[2:3]
	v_lshl_add_u64 v[20:21], v[20:21], 2, s[2:3]
	v_lshl_add_u64 v[26:27], v[26:27], 2, s[2:3]
	v_lshl_add_u64 v[28:29], v[28:29], 2, s[2:3]
	v_lshl_add_u64 v[34:35], v[34:35], 2, s[2:3]
	v_lshl_add_u64 v[36:37], v[36:37], 2, s[2:3]
	v_lshl_add_u64 v[42:43], v[42:43], 2, s[2:3]
	v_lshl_add_u64 v[44:45], v[44:45], 2, s[2:3]
	v_lshl_add_u64 v[50:51], v[50:51], 2, s[2:3]
	v_lshl_add_u64 v[52:53], v[52:53], 2, s[2:3]
	v_lshl_add_u64 v[58:59], v[58:59], 2, s[2:3]
	v_lshl_add_u64 v[60:61], v[60:61], 2, s[2:3]
	v_lshl_add_u64 v[2:3], v[2:3], 0, v[134:135]
	v_lshl_add_u64 v[6:7], v[4:5], 0, v[134:135]
	v_lshl_add_u64 v[10:11], v[10:11], 0, v[134:135]
	v_lshl_add_u64 v[14:15], v[12:13], 0, v[134:135]
	v_lshl_add_u64 v[18:19], v[18:19], 0, v[134:135]
	v_lshl_add_u64 v[22:23], v[20:21], 0, v[134:135]
	v_lshl_add_u64 v[26:27], v[26:27], 0, v[134:135]
	v_lshl_add_u64 v[30:31], v[28:29], 0, v[134:135]
	v_lshl_add_u64 v[34:35], v[34:35], 0, v[134:135]
	v_lshl_add_u64 v[38:39], v[36:37], 0, v[134:135]
	v_lshl_add_u64 v[42:43], v[42:43], 0, v[134:135]
	v_lshl_add_u64 v[46:47], v[44:45], 0, v[134:135]
	v_lshl_add_u64 v[50:51], v[50:51], 0, v[134:135]
	v_lshl_add_u64 v[54:55], v[52:53], 0, v[134:135]
	v_lshl_add_u64 v[58:59], v[58:59], 0, v[134:135]
	v_lshl_add_u64 v[62:63], v[60:61], 0, v[134:135]
	global_load_dwordx4 v[2:5], v[2:3], off nt
	s_nop 0
	global_load_dwordx4 v[6:9], v[6:7], off nt
	s_nop 0
	global_load_dwordx4 v[10:13], v[10:11], off nt
	s_nop 0
	global_load_dwordx4 v[14:17], v[14:15], off nt
	s_nop 0
	global_load_dwordx4 v[18:21], v[18:19], off nt
	s_nop 0
	global_load_dwordx4 v[22:25], v[22:23], off nt
	s_nop 0
	global_load_dwordx4 v[26:29], v[26:27], off nt
	s_nop 0
	global_load_dwordx4 v[30:33], v[30:31], off nt
	s_nop 0
	global_load_dwordx4 v[34:37], v[34:35], off nt
	s_nop 0
	global_load_dwordx4 v[38:41], v[38:39], off nt
	s_nop 0
	global_load_dwordx4 v[42:45], v[42:43], off nt
	s_nop 0
	global_load_dwordx4 v[46:49], v[46:47], off nt
	s_nop 0
	global_load_dwordx4 v[50:53], v[50:51], off nt
	s_nop 0
	global_load_dwordx4 v[54:57], v[54:55], off nt
	s_nop 0
	global_load_dwordx4 v[58:61], v[58:59], off nt
	s_nop 0
	global_load_dwordx4 v[62:65], v[62:63], off nt
; #define GAS __attribute__((address_space(1)))
; #define LAS __attribute__((address_space(3)))
; #define LDS_WAIT() asm volatile("s_waitcnt lgkmcnt(0)" ::: "memory")
; __device__ __forceinline__ unsigned pk4_fp8(float a, float b, float c, float d) { int p = 0; p = __builtin_amdgcn_cvt_pk_fp8_f32(a, b, p, false); p = __builtin_amdgcn_cvt_pk_fp8_f32(c, d, p, true); return (unsigned)p; }
; __device__ __forceinline__ float clamp8s(float x) { return __builtin_amdgcn_fmed3f(x * W8_SCALE, -448.0f, 448.0f); }
; __device__ __forceinline__ void cv_finish(const CvItem& m, int lane, const f32x4 (&v)[16], LAS float* scr) {
;     const int rr = lane >> 3, c4 = (lane & 7) * 4;
; #pragma unroll
;     for (int i = 0; i < 16; ++i) *(LAS f32x4*)(scr + (8 * i + rr) * 36 + (c4 ^ (4 * ((i >> 1) & 7)))) = v[i];
;     LDS_WAIT(); asm volatile("" ::: "memory");
;     const int kc = lane & 7, nn = lane >> 3;
; #pragma unroll
;     for (int j = 0; j < 4; ++j) { const int n = nn + 8 * j; const LAS float* s = scr + (16 * kc) * 36 + (n ^ (4 * kc));
;         float x[16];
; #pragma unroll
;         for (int q = 0; q < 16; ++q) x[q] = s[q * 36];
;         if (m.f8) { v4u o;
;             o.x = pk4_fp8(clamp8s(x[0]), clamp8s(x[1]), clamp8s(x[2]), clamp8s(x[3])); o.y = pk4_fp8(clamp8s(x[4]), clamp8s(x[5]), clamp8s(x[6]), clamp8s(x[7]));
;             o.z = pk4_fp8(clamp8s(x[8]), clamp8s(x[9]), clamp8s(x[10]), clamp8s(x[11])); o.w = pk4_fp8(clamp8s(x[12]), clamp8s(x[13]), clamp8s(x[14]), clamp8s(x[15]));
;             __builtin_nontemporal_store(o, (GAS v4u*)((unsigned char*)m.dst + (size_t)n * m.ldt + 16 * kc)); }
.LBB0_1128:
	s_cmp_gt_i32 s54, 0x15cff
	v_add_u32_e32 v161, 0x400, v151
	v_add_u32_e32 v163, 0x600, v151
	s_cbranch_scc1 .LBB0_1142
	s_waitcnt vmcnt(31)
	ds_write_b128 v1, v[66:69]
	s_waitcnt vmcnt(30)
	ds_write_b128 v131, v[70:73]
	s_waitcnt vmcnt(29)
	ds_write_b128 v133, v[74:77]
	s_waitcnt vmcnt(28)
	ds_write_b128 v137, v[78:81]
	s_waitcnt vmcnt(27)
	ds_write_b128 v139, v[82:85] offset:4608
	s_waitcnt vmcnt(26)
	ds_write_b128 v139, v[86:89] offset:5760
	s_waitcnt vmcnt(25)
	ds_write_b128 v141, v[90:93] offset:6912
	s_waitcnt vmcnt(24)
	ds_write_b128 v141, v[94:97] offset:8064
	s_waitcnt vmcnt(23)
	ds_write_b128 v143, v[98:101] offset:9216
	s_waitcnt vmcnt(22)
	ds_write_b128 v143, v[102:105] offset:10368
	s_waitcnt vmcnt(21)
	ds_write_b128 v145, v[106:109] offset:11520
	s_waitcnt vmcnt(20)
	ds_write_b128 v145, v[110:113] offset:12672
	s_waitcnt vmcnt(19)
	ds_write_b128 v147, v[114:117] offset:13824
	s_waitcnt vmcnt(18)
	ds_write_b128 v147, v[118:121] offset:14976
	s_waitcnt vmcnt(17)
	ds_write_b128 v149, v[122:125] offset:16128
	s_waitcnt vmcnt(16)
	ds_write_b128 v149, v[126:129] offset:17280
	s_waitcnt lgkmcnt(0)
	ds_read2_b32 v[182:183], v151 offset1:36
	ds_read2_b32 v[180:181], v151 offset0:72 offset1:108
	ds_read2_b32 v[178:179], v151 offset0:144 offset1:180
	ds_read2_b32 v[176:177], v151 offset0:216 offset1:252
	ds_read2_b32 v[174:175], v161 offset0:32 offset1:68
	ds_read2_b32 v[172:173], v161 offset0:104 offset1:140
	ds_read2_b32 v[170:171], v161 offset0:176 offset1:212
	ds_read2_b32 v[168:169], v163 offset0:120 offset1:156
	s_cmp_lg_u32 s46, 0
	s_cselect_b64 s[16:17], -1, 0
	s_cmp_eq_u32 s46, 0
	s_cbranch_scc1 .LBB0_1175
	s_waitcnt lgkmcnt(7)
	v_mul_f32_e32 v134, 0x42800000, v182
	v_mul_f32_e32 v165, 0x42800000, v183
	v_med3_f32 v134, v134, s41, v159
	v_med3_f32 v165, v165, s41, v159
	v_mov_b32_e32 v184, v135
	v_cvt_pk_fp8_f32 v184, v134, v165
	s_waitcnt lgkmcnt(6)
	v_mul_f32_e32 v185, 0x42800000, v180
	v_mul_f32_e32 v165, 0x42800000, v181
	v_med3_f32 v134, v185, s41, v159
	v_med3_f32 v165, v165, s41, v159
	v_cvt_pk_fp8_f32 v184, v134, v165 op_sel:[0,0,1]
	s_waitcnt lgkmcnt(5)
	v_mul_f32_e32 v134, 0x42800000, v178
	v_mul_f32_e32 v165, 0x42800000, v179
	v_med3_f32 v134, v134, s41, v159
	v_med3_f32 v165, v165, s41, v159
	v_mov_b32_e32 v185, v135
	v_cvt_pk_fp8_f32 v185, v134, v165
	s_waitcnt lgkmcnt(4)
	v_mul_f32_e32 v186, 0x42800000, v176
	v_mul_f32_e32 v165, 0x42800000, v177
	v_med3_f32 v134, v186, s41, v159
	v_med3_f32 v165, v165, s41, v159
	v_cvt_pk_fp8_f32 v185, v134, v165 op_sel:[0,0,1]
	s_waitcnt lgkmcnt(3)
	v_mul_f32_e32 v134, 0x42800000, v174
	v_mul_f32_e32 v165, 0x42800000, v175
	v_med3_f32 v134, v134, s41, v159
	v_med3_f32 v165, v165, s41, v159
	v_mov_b32_e32 v186, v135
	v_cvt_pk_fp8_f32 v186, v134, v165
	s_waitcnt lgkmcnt(2)
	v_mul_f32_e32 v187, 0x42800000, v172
	v_mul_f32_e32 v165, 0x42800000, v173
	v_med3_f32 v134, v187, s41, v159
	v_med3_f32 v165, v165, s41, v159
	v_cvt_pk_fp8_f32 v186, v134, v165 op_sel:[0,0,1]
	s_waitcnt lgkmcnt(1)
	v_mul_f32_e32 v134, 0x42800000, v170
	v_mul_f32_e32 v165, 0x42800000, v171
	v_med3_f32 v134, v134, s41, v159
	v_med3_f32 v165, v165, s41, v159
	v_mov_b32_e32 v187, v135
	v_cvt_pk_fp8_f32 v187, v134, v165
	s_waitcnt lgkmcnt(0)
	v_mul_f32_e32 v188, 0x42800000, v168
	v_mul_f32_e32 v165, 0x42800000, v169
	v_med3_f32 v134, v188, s41, v159
	v_med3_f32 v165, v165, s41, v159
	v_cvt_pk_fp8_f32 v187, v134, v165 op_sel:[0,0,1]
	v_mov_b64_e32 v[188:189], s[12:13]
	v_mad_i64_i32 v[188:189], s[2:3], s45, v130, v[188:189]
	v_lshl_add_u64 v[188:189], v[188:189], 0, v[166:167]
	global_store_dwordx4 v[188:189], v[184:187], off nt
	s_cbranch_execnz .LBB0_1132

; __device__ __forceinline__ CvItem cv_item(Frame& F, int it) {
;     int r = it;
;     if (r < I_WIN0) return cv_make(F.in[7], DM, EIN, WSP(bf16, WS_WIN0), 0, r); r -= I_WIN0;
;     if (r < I_SQ) return cv_make(F.in[11], DM, DM, WSP(bf16, WS_WOUT0), 0, r); r -= I_SQ;
;     if (r < I_F) return cv_make(F.in[13], DM, DFF, WSP(bf16, WS_WGU0), 1, r, FFN8); r -= I_F;
;     if (r < I_F) return cv_make(F.in[14], DM, DFF, WSP(bf16, WS_WGU0), 2, r, FFN8); r -= I_F;
;     if (r < I_F) return cv_make(F.in[15], DFF, DM, WSP(bf16, WS_WD0), 0, r, FFN8); r -= I_F;
;     if (r < I_WIN1) return cv_make(F.in[19], DM, 2 * DM, WSP(bf16, WS_WIN1), 0, r); r -= I_WIN1;
;     if (r < I_SQ) return cv_make(F.in[27], DM, DM, WSP(bf16, WS_WOUT1), 0, r); r -= I_SQ;
;     if (r < 64 * I_G) { const int mtx = r >> 2, sub = r & 3, gt = mtx >> 5, zh = mtx & 31, z = zh >> 4, h = zh & 15;
;         return cv_make(F.in[gt ? 24 : 22] + (size_t)zh * 16384, 128, 128, WSP(bf16, WS_WGT) + (size_t)((z * 2 + gt) * 16 + h) * 16384, 0, sub); } r -= 64 * I_G;
;     const int w = r / (8 * I_ME), rr = r % (8 * I_ME), e = rr / I_ME, sub = rr % I_ME;
;     if (w == 0) return cv_make(F.in[31] + (size_t)e * DM * DFFE, DM, DFFE, (bf16*)(F.ws + WS_MWGU + (size_t)e * 2 * DFFE * DM), 1, sub, 1);
;     if (w == 1) return cv_make(F.in[32] + (size_t)e * DM * DFFE, DM, DFFE, (bf16*)(F.ws + WS_MWGU + (size_t)e * 2 * DFFE * DM), 2, sub, 1);
;     return cv_make(F.in[33] + (size_t)e * DFFE * DM, DFFE, DM, (bf16*)(F.ws + WS_MWD + (size_t)e * DM * DFFE), 0, sub, 1);
; __device__ __forceinline__ void moe_pull(Frame& F, int k, int until) {
;     ...
;         for (int t = 0; t < 8; t += 2) {
;             if (f + t + 1 < NQ) { mb = cv_item(F, NEARLY + f + t + 1); cv_load(mb, F.lane, vb); }
;             if (f + t < NQ) cv_finish(ma, F.lane, va, scr);
;             if (t + 2 < 8 && f + t + 2 < NQ) { ma = cv_item(F, NEARLY + f + t + 2); cv_load(ma, F.lane, va); }
;             if (f + t + 1 < NQ) cv_finish(mb, F.lane, vb, scr);
.LBB0_1142:
	s_cmp_gt_u32 s51, 5
	s_cselect_b64 s[16:17], -1, 0
	s_cmp_gt_i32 s54, 0x15cfd
	s_cselect_b64 s[2:3], -1, 0
	s_or_b64 s[2:3], s[16:17], s[2:3]
	s_and_b64 vcc, exec, s[2:3]
	s_cbranch_vccz .Lcv9_go1
	s_waitcnt vmcnt(0)
	s_branch .LBB0_1163
.Lcv9_go1:
	s_add_i32 s6, s54, 0x2e00
	s_cmpk_gt_u32 s6, 0x35fd
	s_mov_b64 s[20:21], -1
	s_cbranch_scc0 .LBB0_1160
	s_cmpk_gt_u32 s6, 0x39fd
	s_cbranch_scc0 .LBB0_1157
	s_cmpk_gt_u32 s6, 0x3afd
	s_cbranch_scc0 .LBB0_1154
	s_lshr_b32 s2, s53, 12
	s_mul_hi_u32 s2, s2, 0x24924925
	s_mulk_i32 s2, 0x7000
	s_sub_i32 s2, s47, s2
	s_add_i32 s2, s51, s2
	s_bfe_u32 s6, s2, 0x70009
	s_mulk_i32 s6, 0x2493
	s_lshr_b32 s46, s6, 16
	s_mul_i32 s6, s46, 0xe00
	s_add_i32 s3, s54, 0xfffff302
	s_sub_i32 s6, s2, s6
	s_cmpk_gt_u32 s3, 0x6fff
	s_mul_i32 s55, s46, 0x3800000
	s_cbranch_scc0 .LBB0_1151
	s_add_i32 s2, s54, 0xffff8302
	s_cmpk_gt_u32 s2, 0x6fff
	s_mov_b64 s[18:19], -1
	s_cbranch_scc0 .LBB0_1149
	v_readlane_b32 s56, v250, 0
	v_readlane_b32 s58, v250, 2
	v_readlane_b32 s59, v250, 3
	s_add_u32 s2, s58, s55
	s_addc_u32 s3, s59, 0
	s_mul_i32 s12, s46, 0xe00000
	s_add_u32 s12, s23, s12
	s_addc_u32 s13, s24, 0
	s_lshl_b32 s19, s6, 5
	s_lshl_b32 s18, s6, 1
	s_and_b32 s19, s19, 0x7e0
	s_and_b32 s18, s18, 0x1f80
	s_mul_i32 s20, s19, 0x1c00
	s_add_u32 s12, s12, s20
	s_addc_u32 s13, s13, 0
	s_add_u32 s12, s12, s18
	s_addc_u32 s13, s13, 0
	s_lshl_b32 s18, s18, 13
	s_add_u32 s2, s2, s18
	s_addc_u32 s3, s3, 0
	s_lshl_b32 s18, s19, 2
	s_add_u32 s2, s2, s18
	v_readlane_b32 s57, v250, 1
	v_readlane_b32 s60, v250, 4
	v_readlane_b32 s61, v250, 5
	v_readlane_b32 s62, v250, 6
	v_readlane_b32 s63, v250, 7
	s_addc_u32 s3, s3, 0
	s_mov_b64 s[18:19], 0

; #define GAS __attribute__((address_space(1)))
; __device__ __forceinline__ void cv_load(const CvItem& m, int lane, f32x4 (&v)[16]) {
;     const int rr = lane >> 3, c4 = (lane & 7) * 4;
; #pragma unroll
;     for (int i = 0; i < 16; ++i) v[i] = __builtin_nontemporal_load((const GAS f32x4*)(m.src + (size_t)(8 * i + rr) * m.ldw + c4));
; }
.LBB0_1162:
	v_mad_u64_u32 v[66:67], s[20:21], s18, v130, 0
	v_mad_u64_u32 v[74:75], s[20:21], s18, v138, 0
	v_mad_u64_u32 v[82:83], s[20:21], s18, v142, 0
	v_mad_u64_u32 v[90:91], s[20:21], s18, v146, 0
	v_mad_u64_u32 v[98:99], s[20:21], s18, v150, 0
	v_mad_u64_u32 v[106:107], s[20:21], s18, v154, 0
	v_mad_u64_u32 v[114:115], s[20:21], s18, v158, 0
	v_mad_u64_u32 v[122:123], s[20:21], s18, v162, 0
	v_mov_b32_e32 v68, v67
	v_mov_b32_e32 v76, v75
	v_mov_b32_e32 v84, v83
	v_mov_b32_e32 v92, v91
	v_mov_b32_e32 v100, v99
	v_mov_b32_e32 v108, v107
	v_mov_b32_e32 v116, v115
	v_mov_b32_e32 v124, v123
	v_mad_u64_u32 v[68:69], s[20:21], s19, v130, v[68:69]
	v_mad_u64_u32 v[76:77], s[20:21], s19, v138, v[76:77]
	v_mad_u64_u32 v[84:85], s[20:21], s19, v142, v[84:85]
	v_mad_u64_u32 v[92:93], s[20:21], s19, v146, v[92:93]
	v_mad_u64_u32 v[100:101], s[20:21], s19, v150, v[100:101]
	v_mad_u64_u32 v[108:109], s[20:21], s19, v154, v[108:109]
	v_mad_u64_u32 v[116:117], s[20:21], s19, v158, v[116:117]
	v_mad_u64_u32 v[124:125], s[20:21], s19, v162, v[124:125]
	v_mov_b32_e32 v67, v68
	v_mad_u64_u32 v[68:69], s[20:21], s18, v136, 0
	v_mov_b32_e32 v75, v76
	v_mad_u64_u32 v[76:77], s[20:21], s18, v140, 0
	v_mov_b32_e32 v83, v84
	v_mad_u64_u32 v[84:85], s[20:21], s18, v144, 0
	v_mov_b32_e32 v91, v92
	v_mad_u64_u32 v[92:93], s[20:21], s18, v148, 0
	v_mov_b32_e32 v99, v100
	v_mad_u64_u32 v[100:101], s[20:21], s18, v152, 0
	v_mov_b32_e32 v107, v108
	v_mad_u64_u32 v[108:109], s[20:21], s18, v156, 0
	v_mov_b32_e32 v115, v116
	v_mad_u64_u32 v[116:117], s[20:21], s18, v160, 0
	v_mov_b32_e32 v123, v124
	v_mad_u64_u32 v[124:125], s[20:21], s18, v164, 0
	v_mov_b32_e32 v70, v69
	v_mov_b32_e32 v78, v77
	v_mov_b32_e32 v86, v85
	v_mov_b32_e32 v94, v93
	v_mov_b32_e32 v102, v101
	v_mov_b32_e32 v110, v109
	v_mov_b32_e32 v118, v117
	v_mov_b32_e32 v126, v125
	v_mad_u64_u32 v[70:71], s[20:21], s19, v136, v[70:71]
	v_mad_u64_u32 v[78:79], s[20:21], s19, v140, v[78:79]
	v_mad_u64_u32 v[86:87], s[20:21], s19, v144, v[86:87]
	v_mad_u64_u32 v[94:95], s[20:21], s19, v148, v[94:95]
	v_mad_u64_u32 v[102:103], s[20:21], s19, v152, v[102:103]
	v_mad_u64_u32 v[110:111], s[20:21], s19, v156, v[110:111]
	v_mad_u64_u32 v[118:119], s[20:21], s19, v160, v[118:119]
	v_mad_u64_u32 v[126:127], s[18:19], s19, v164, v[126:127]
	v_mov_b32_e32 v69, v70
	v_mov_b32_e32 v77, v78
	v_mov_b32_e32 v85, v86
	v_mov_b32_e32 v93, v94
	v_mov_b32_e32 v101, v102
	v_mov_b32_e32 v109, v110
	v_mov_b32_e32 v117, v118
	v_mov_b32_e32 v125, v126
	v_lshl_add_u64 v[66:67], v[66:67], 2, s[2:3]
	v_lshlrev_b32_e32 v134, 2, v132
	v_lshl_add_u64 v[68:69], v[68:69], 2, s[2:3]
	v_lshl_add_u64 v[74:75], v[74:75], 2, s[2:3]
	v_lshl_add_u64 v[76:77], v[76:77], 2, s[2:3]
	v_lshl_add_u64 v[82:83], v[82:83], 2, s[2:3]
	v_lshl_add_u64 v[84:85], v[84:85], 2, s[2:3]
	v_lshl_add_u64 v[90:91], v[90:91], 2, s[2:3]
	v_lshl_add_u64 v[92:93], v[92:93], 2, s[2:3]
	v_lshl_add_u64 v[98:99], v[98:99], 2, s[2:3]
	v_lshl_add_u64 v[100:101], v[100:101], 2, s[2:3]
	v_lshl_add_u64 v[106:107], v[106:107], 2, s[2:3]
	v_lshl_add_u64 v[108:109], v[108:109], 2, s[2:3]
	v_lshl_add_u64 v[114:115], v[114:115], 2, s[2:3]
	v_lshl_add_u64 v[116:117], v[116:117], 2, s[2:3]
	v_lshl_add_u64 v[122:123], v[122:123], 2, s[2:3]
	v_lshl_add_u64 v[124:125], v[124:125], 2, s[2:3]
	v_lshl_add_u64 v[66:67], v[66:67], 0, v[134:135]
	v_lshl_add_u64 v[70:71], v[68:69], 0, v[134:135]
	v_lshl_add_u64 v[74:75], v[74:75], 0, v[134:135]
	v_lshl_add_u64 v[78:79], v[76:77], 0, v[134:135]
	v_lshl_add_u64 v[82:83], v[82:83], 0, v[134:135]
	v_lshl_add_u64 v[86:87], v[84:85], 0, v[134:135]
	v_lshl_add_u64 v[90:91], v[90:91], 0, v[134:135]
	v_lshl_add_u64 v[94:95], v[92:93], 0, v[134:135]
	v_lshl_add_u64 v[98:99], v[98:99], 0, v[134:135]
	v_lshl_add_u64 v[102:103], v[100:101], 0, v[134:135]
	v_lshl_add_u64 v[106:107], v[106:107], 0, v[134:135]
	v_lshl_add_u64 v[110:111], v[108:109], 0, v[134:135]
	v_lshl_add_u64 v[114:115], v[114:115], 0, v[134:135]
	v_lshl_add_u64 v[118:119], v[116:117], 0, v[134:135]
	v_lshl_add_u64 v[122:123], v[122:123], 0, v[134:135]
	v_lshl_add_u64 v[126:127], v[124:125], 0, v[134:135]
	global_load_dwordx4 v[66:69], v[66:67], off nt
	s_nop 0
	global_load_dwordx4 v[70:73], v[70:71], off nt
	s_nop 0
	global_load_dwordx4 v[74:77], v[74:75], off nt
	s_nop 0
	global_load_dwordx4 v[78:81], v[78:79], off nt
	s_nop 0
	global_load_dwordx4 v[82:85], v[82:83], off nt
	s_nop 0
	global_load_dwordx4 v[86:89], v[86:87], off nt
	s_nop 0
	global_load_dwordx4 v[90:93], v[90:91], off nt
	s_nop 0
	global_load_dwordx4 v[94:97], v[94:95], off nt
	s_nop 0
	global_load_dwordx4 v[98:101], v[98:99], off nt
	s_nop 0
	global_load_dwordx4 v[102:105], v[102:103], off nt
	s_nop 0
	global_load_dwordx4 v[106:109], v[106:107], off nt
	s_nop 0
	global_load_dwordx4 v[110:113], v[110:111], off nt
	s_nop 0
	global_load_dwordx4 v[114:117], v[114:115], off nt
	s_nop 0
	global_load_dwordx4 v[118:121], v[118:119], off nt
	s_nop 0
	global_load_dwordx4 v[122:125], v[122:123], off nt
	s_nop 0
	global_load_dwordx4 v[126:129], v[126:127], off nt
; #define GAS __attribute__((address_space(1)))
; #define LAS __attribute__((address_space(3)))
; #define LDS_WAIT() asm volatile("s_waitcnt lgkmcnt(0)" ::: "memory")
; __device__ __forceinline__ unsigned pk4_fp8(float a, float b, float c, float d) { int p = 0; p = __builtin_amdgcn_cvt_pk_fp8_f32(a, b, p, false); p = __builtin_amdgcn_cvt_pk_fp8_f32(c, d, p, true); return (unsigned)p; }
; __device__ __forceinline__ float clamp8s(float x) { return __builtin_amdgcn_fmed3f(x * W8_SCALE, -448.0f, 448.0f); }
; __device__ __forceinline__ void cv_finish(const CvItem& m, int lane, const f32x4 (&v)[16], LAS float* scr) {
;     const int rr = lane >> 3, c4 = (lane & 7) * 4;
; #pragma unroll
;     for (int i = 0; i < 16; ++i) *(LAS f32x4*)(scr + (8 * i + rr) * 36 + (c4 ^ (4 * ((i >> 1) & 7)))) = v[i];
;     LDS_WAIT(); asm volatile("" ::: "memory");
;     const int kc = lane & 7, nn = lane >> 3;
; #pragma unroll
;     for (int j = 0; j < 4; ++j) { const int n = nn + 8 * j; const LAS float* s = scr + (16 * kc) * 36 + (n ^ (4 * kc));
;         float x[16];
; #pragma unroll
;         for (int q = 0; q < 16; ++q) x[q] = s[q * 36];
;         if (m.f8) { v4u o;
;             o.x = pk4_fp8(clamp8s(x[0]), clamp8s(x[1]), clamp8s(x[2]), clamp8s(x[3])); o.y = pk4_fp8(clamp8s(x[4]), clamp8s(x[5]), clamp8s(x[6]), clamp8s(x[7]));
;             o.z = pk4_fp8(clamp8s(x[8]), clamp8s(x[9]), clamp8s(x[10]), clamp8s(x[11])); o.w = pk4_fp8(clamp8s(x[12]), clamp8s(x[13]), clamp8s(x[14]), clamp8s(x[15]));
;             __builtin_nontemporal_store(o, (GAS v4u*)((unsigned char*)m.dst + (size_t)n * m.ldt + 16 * kc)); }
.LBB0_1163:
	s_andn2_b64 vcc, exec, s[14:15]
	s_cbranch_vccnz .LBB0_1102
	s_waitcnt vmcnt(31)
	ds_write_b128 v1, v[2:5]
	s_waitcnt vmcnt(30)
	ds_write_b128 v131, v[6:9]
	s_waitcnt vmcnt(29)
	ds_write_b128 v133, v[10:13]
	s_waitcnt vmcnt(28)
	ds_write_b128 v137, v[14:17]
	s_waitcnt vmcnt(27)
	ds_write_b128 v139, v[18:21] offset:4608
	s_waitcnt vmcnt(26)
	ds_write_b128 v139, v[22:25] offset:5760
	s_waitcnt vmcnt(25)
	ds_write_b128 v141, v[26:29] offset:6912
	s_waitcnt vmcnt(24)
	ds_write_b128 v141, v[30:33] offset:8064
	s_waitcnt vmcnt(23)
	ds_write_b128 v143, v[34:37] offset:9216
	s_waitcnt vmcnt(22)
	ds_write_b128 v143, v[38:41] offset:10368
	s_waitcnt vmcnt(21)
	ds_write_b128 v145, v[42:45] offset:11520
	s_waitcnt vmcnt(20)
	ds_write_b128 v145, v[46:49] offset:12672
	s_waitcnt vmcnt(19)
	ds_write_b128 v147, v[50:53] offset:13824
	s_waitcnt vmcnt(18)
	ds_write_b128 v147, v[54:57] offset:14976
	s_waitcnt vmcnt(17)
	ds_write_b128 v149, v[58:61] offset:16128
	s_waitcnt vmcnt(16)
	ds_write_b128 v149, v[62:65] offset:17280
	s_waitcnt lgkmcnt(0)
	s_waitcnt lgkmcnt(14)
	ds_read2_b32 v[182:183], v151 offset1:36
	ds_read2_b32 v[180:181], v151 offset0:72 offset1:108
	ds_read2_b32 v[178:179], v151 offset0:144 offset1:180
	ds_read2_b32 v[176:177], v151 offset0:216 offset1:252
	ds_read2_b32 v[174:175], v161 offset0:32 offset1:68
	ds_read2_b32 v[172:173], v161 offset0:104 offset1:140
	ds_read2_b32 v[170:171], v161 offset0:176 offset1:212
	ds_read2_b32 v[168:169], v163 offset0:120 offset1:156
	s_cmp_lg_u32 s44, 0
	s_cselect_b64 s[14:15], -1, 0
	s_cmp_eq_u32 s44, 0
	s_cbranch_scc1 .LBB0_1179
	s_waitcnt lgkmcnt(7)
	v_mul_f32_e32 v134, 0x42800000, v182
	v_mul_f32_e32 v161, 0x42800000, v183
	v_med3_f32 v134, v134, s41, v159
	v_med3_f32 v161, v161, s41, v159
	v_mov_b32_e32 v184, v135
	v_cvt_pk_fp8_f32 v184, v134, v161
	s_waitcnt lgkmcnt(6)
	v_mul_f32_e32 v163, 0x42800000, v180
	v_mul_f32_e32 v161, 0x42800000, v181
	v_med3_f32 v134, v163, s41, v159
	v_med3_f32 v161, v161, s41, v159
	v_cvt_pk_fp8_f32 v184, v134, v161 op_sel:[0,0,1]
	s_waitcnt lgkmcnt(5)
	v_mul_f32_e32 v134, 0x42800000, v178
	v_mul_f32_e32 v161, 0x42800000, v179
	v_med3_f32 v134, v134, s41, v159
	v_med3_f32 v161, v161, s41, v159
	v_mov_b32_e32 v185, v135
	v_cvt_pk_fp8_f32 v185, v134, v161
	s_waitcnt lgkmcnt(4)
	v_mul_f32_e32 v163, 0x42800000, v176
	v_mul_f32_e32 v161, 0x42800000, v177
	v_med3_f32 v134, v163, s41, v159
	v_med3_f32 v161, v161, s41, v159
	v_cvt_pk_fp8_f32 v185, v134, v161 op_sel:[0,0,1]
	s_waitcnt lgkmcnt(3)
	v_mul_f32_e32 v134, 0x42800000, v174
	v_mul_f32_e32 v161, 0x42800000, v175
	v_med3_f32 v134, v134, s41, v159
	v_med3_f32 v161, v161, s41, v159
	v_mov_b32_e32 v186, v135
	v_cvt_pk_fp8_f32 v186, v134, v161
	s_waitcnt lgkmcnt(2)
	v_mul_f32_e32 v163, 0x42800000, v172
	v_mul_f32_e32 v161, 0x42800000, v173
	v_med3_f32 v134, v163, s41, v159
	v_med3_f32 v161, v161, s41, v159
	v_cvt_pk_fp8_f32 v186, v134, v161 op_sel:[0,0,1]
	s_waitcnt lgkmcnt(1)
	v_mul_f32_e32 v134, 0x42800000, v170
	v_mul_f32_e32 v161, 0x42800000, v171
	v_med3_f32 v134, v134, s41, v159
	v_med3_f32 v161, v161, s41, v159
	v_mov_b32_e32 v187, v135
	v_cvt_pk_fp8_f32 v187, v134, v161
	s_waitcnt lgkmcnt(0)
	v_mul_f32_e32 v163, 0x42800000, v168
	v_mul_f32_e32 v161, 0x42800000, v169
	v_med3_f32 v134, v163, s41, v159
	v_med3_f32 v161, v161, s41, v159
	v_cvt_pk_fp8_f32 v187, v134, v161 op_sel:[0,0,1]
	v_mov_b64_e32 v[188:189], s[10:11]
	v_mad_i64_i32 v[188:189], s[2:3], s42, v130, v[188:189]
	v_lshl_add_u64 v[188:189], v[188:189], 0, v[166:167]
	global_store_dwordx4 v[188:189], v[184:187], off nt
	v_lshlrev_b32_e32 v134, 1, v166
	s_cbranch_execnz .LBB0_1167

;     const int nb = N / 32, kb = sub / nb, nbi = sub % nb, k0 = kb * 128, n0 = nbi * 32;
;     const int dr = mode == 0 ? n0 : (256 * (n0 >> 7) + (n0 & 127) + (mode == 2 ? 128 : 0));
;     CvItem m; m.src = W + (size_t)k0 * N + n0; m.ldw = N; m.f8 = f8;
;     if (f8) { m.dst = (bf16*)((unsigned char*)WT + (size_t)dr * K + k0); m.ldt = K; } else { m.dst = WT + (size_t)dr * K + k0; m.ldt = K; }
;     return m;
; }
; __device__ __forceinline__ CvItem cv_item(Frame& F, int it) {
;     int r = it;
;     if (r < I_WIN0) return cv_make(F.in[7], DM, EIN, WSP(bf16, WS_WIN0), 0, r); r -= I_WIN0;
;     if (r < I_SQ) return cv_make(F.in[11], DM, DM, WSP(bf16, WS_WOUT0), 0, r); r -= I_SQ;
;     if (r < I_F) return cv_make(F.in[13], DM, DFF, WSP(bf16, WS_WGU0), 1, r, FFN8); r -= I_F;
;     if (r < I_F) return cv_make(F.in[14], DM, DFF, WSP(bf16, WS_WGU0), 2, r, FFN8); r -= I_F;
;     if (r < I_F) return cv_make(F.in[15], DFF, DM, WSP(bf16, WS_WD0), 0, r, FFN8); r -= I_F;
;     if (r < I_WIN1) return cv_make(F.in[19], DM, 2 * DM, WSP(bf16, WS_WIN1), 0, r); r -= I_WIN1;
;     if (r < I_SQ) return cv_make(F.in[27], DM, DM, WSP(bf16, WS_WOUT1), 0, r); r -= I_SQ;
;     if (r < 64 * I_G) { const int mtx = r >> 2, sub = r & 3, gt = mtx >> 5, zh = mtx & 31, z = zh >> 4, h = zh & 15;
;         return cv_make(F.in[gt ? 24 : 22] + (size_t)zh * 16384, 128, 128, WSP(bf16, WS_WGT) + (size_t)((z * 2 + gt) * 16 + h) * 16384, 0, sub); } r -= 64 * I_G;
;     const int w = r / (8 * I_ME), rr = r % (8 * I_ME), e = rr / I_ME, sub = rr % I_ME;
;     if (w == 0) return cv_make(F.in[31] + (size_t)e * DM * DFFE, DM, DFFE, (bf16*)(F.ws + WS_MWGU + (size_t)e * 2 * DFFE * DM), 1, sub, 1);
;     if (w == 1) return cv_make(F.in[32] + (size_t)e * DM * DFFE, DM, DFFE, (bf16*)(F.ws + WS_MWGU + (size_t)e * 2 * DFFE * DM), 2, sub, 1);
;     return cv_make(F.in[33] + (size_t)e * DFFE * DM, DFFE, DM, (bf16*)(F.ws + WS_MWD + (size_t)e * DM * DFFE), 0, sub, 1);
; __device__ __forceinline__ void moe_pull(Frame& F, int k, int until) {
;     ...
;         for (int t = 0; t < 8; t += 2) {
;             if (f + t + 1 < NQ) { mb = cv_item(F, NEARLY + f + t + 1); cv_load(mb, F.lane, vb); }
.LBB0_1788:
	s_add_i32 s54, s43, s51
	s_cmp_lt_i32 s54, 0x15cff
	s_cselect_b64 s[12:13], -1, 0
	s_cmp_gt_i32 s54, 0x15cfe
	s_cbranch_scc0 .Lcv15_go0
	s_waitcnt vmcnt(0)
	s_branch .LBB0_1813
.Lcv15_go0:
	s_add_i32 s4, s54, 0x2e00
	s_add_i32 s18, s54, 0x2e01
	s_cmpk_gt_i32 s4, 0x8fe
	s_mov_b64 s[16:17], -1
	s_cbranch_scc0 .LBB0_1810
	s_cmpk_gt_u32 s4, 0x35fe
	s_cbranch_scc0 .LBB0_1807
	s_cmpk_gt_u32 s4, 0x39fe
	s_cbranch_scc0 .LBB0_1804
	s_cmpk_gt_u32 s4, 0x3afe
	s_cbranch_scc0 .LBB0_1801
	s_lshr_b32 s2, s52, 12
	s_mul_hi_u32 s2, s2, 0x24924925
	s_mulk_i32 s2, 0x7000
	s_sub_i32 s2, s50, s2
	s_add_i32 s2, s51, s2
	s_bfe_u32 s4, s2, 0x70009
	s_mulk_i32 s4, 0x2493
	s_lshr_b32 s19, s4, 16
	s_mul_i32 s4, s19, 0xe00
	s_add_i32 s3, s54, 0xfffff301
	s_sub_i32 s4, s2, s4
	s_cmpk_gt_u32 s3, 0x6fff
	s_mul_i32 s44, s19, 0x3800000
	s_cbranch_scc0 .LBB0_1798
	s_add_i32 s2, s54, 0xffff8301
	s_cmpk_gt_u32 s2, 0x6fff
	s_mov_b64 s[14:15], -1
	s_cbranch_scc0 .LBB0_1796
	v_readlane_b32 s56, v250, 0
	v_readlane_b32 s58, v250, 2
	v_readlane_b32 s59, v250, 3
	s_add_u32 s2, s58, s44
	s_addc_u32 s3, s59, 0
	s_mul_i32 s8, s19, 0xe00000
	s_add_u32 s8, s21, s8
	s_addc_u32 s9, s22, 0
	s_lshl_b32 s15, s4, 5
	s_lshl_b32 s14, s4, 1
	s_and_b32 s15, s15, 0x7e0
	s_and_b32 s14, s14, 0x1f80
	s_mul_i32 s16, s15, 0x1c00
	s_add_u32 s8, s8, s16
	s_addc_u32 s9, s9, 0
	s_add_u32 s8, s8, s14
	s_addc_u32 s9, s9, 0
	s_lshl_b32 s14, s14, 13
	s_add_u32 s2, s2, s14
	s_addc_u32 s3, s3, 0
	s_lshl_b32 s14, s15, 2
	s_add_u32 s2, s2, s14
	v_readlane_b32 s57, v250, 1
	v_readlane_b32 s60, v250, 4
	v_readlane_b32 s61, v250, 5
	v_readlane_b32 s62, v250, 6
	v_readlane_b32 s63, v250, 7
	s_addc_u32 s3, s3, 0
	s_mov_b64 s[14:15], 0

; #define GAS __attribute__((address_space(1)))
; __device__ __forceinline__ void cv_load(const CvItem& m, int lane, f32x4 (&v)[16]) {
;     const int rr = lane >> 3, c4 = (lane & 7) * 4;
; #pragma unroll
;     for (int i = 0; i < 16; ++i) v[i] = __builtin_nontemporal_load((const GAS f32x4*)(m.src + (size_t)(8 * i + rr) * m.ldw + c4));
; }
.LBB0_1812:
	v_mad_u64_u32 v[2:3], s[16:17], s14, v130, 0
	v_mad_u64_u32 v[10:11], s[16:17], s14, v138, 0
	v_mad_u64_u32 v[18:19], s[16:17], s14, v142, 0
	v_mad_u64_u32 v[26:27], s[16:17], s14, v146, 0
	v_mad_u64_u32 v[34:35], s[16:17], s14, v150, 0
	v_mad_u64_u32 v[42:43], s[16:17], s14, v154, 0
	v_mad_u64_u32 v[50:51], s[16:17], s14, v158, 0
	v_mad_u64_u32 v[58:59], s[16:17], s14, v162, 0
	v_mov_b32_e32 v4, v3
	v_mov_b32_e32 v12, v11
	v_mov_b32_e32 v20, v19
	v_mov_b32_e32 v28, v27
	v_mov_b32_e32 v36, v35
	v_mov_b32_e32 v44, v43
	v_mov_b32_e32 v52, v51
	v_mov_b32_e32 v60, v59
	v_mad_u64_u32 v[4:5], s[16:17], s15, v130, v[4:5]
	v_mad_u64_u32 v[12:13], s[16:17], s15, v138, v[12:13]
	v_mad_u64_u32 v[20:21], s[16:17], s15, v142, v[20:21]
	v_mad_u64_u32 v[28:29], s[16:17], s15, v146, v[28:29]
	v_mad_u64_u32 v[36:37], s[16:17], s15, v150, v[36:37]
	v_mad_u64_u32 v[44:45], s[16:17], s15, v154, v[44:45]
	v_mad_u64_u32 v[52:53], s[16:17], s15, v158, v[52:53]
	v_mad_u64_u32 v[60:61], s[16:17], s15, v162, v[60:61]
	v_mov_b32_e32 v3, v4
	v_mad_u64_u32 v[4:5], s[16:17], s14, v136, 0
	v_mov_b32_e32 v11, v12
	v_mad_u64_u32 v[12:13], s[16:17], s14, v140, 0
	v_mov_b32_e32 v19, v20
	v_mad_u64_u32 v[20:21], s[16:17], s14, v144, 0
	v_mov_b32_e32 v27, v28
	v_mad_u64_u32 v[28:29], s[16:17], s14, v148, 0
	v_mov_b32_e32 v35, v36
	v_mad_u64_u32 v[36:37], s[16:17], s14, v152, 0
	v_mov_b32_e32 v43, v44
	v_mad_u64_u32 v[44:45], s[16:17], s14, v156, 0
	v_mov_b32_e32 v51, v52
	v_mad_u64_u32 v[52:53], s[16:17], s14, v160, 0
	v_mov_b32_e32 v59, v60
	v_mad_u64_u32 v[60:61], s[16:17], s14, v164, 0
	v_mov_b32_e32 v6, v5
	v_mov_b32_e32 v14, v13
	v_mov_b32_e32 v22, v21
	v_mov_b32_e32 v30, v29
	v_mov_b32_e32 v38, v37
	v_mov_b32_e32 v46, v45
	v_mov_b32_e32 v54, v53
	v_mov_b32_e32 v62, v61
	v_mad_u64_u32 v[6:7], s[16:17], s15, v136, v[6:7]
	v_mad_u64_u32 v[14:15], s[16:17], s15, v140, v[14:15]
	v_mad_u64_u32 v[22:23], s[16:17], s15, v144, v[22:23]
	v_mad_u64_u32 v[30:31], s[16:17], s15, v148, v[30:31]
	v_mad_u64_u32 v[38:39], s[16:17], s15, v152, v[38:39]
	v_mad_u64_u32 v[46:47], s[16:17], s15, v156, v[46:47]
	v_mad_u64_u32 v[54:55], s[16:17], s15, v160, v[54:55]
	v_mad_u64_u32 v[62:63], s[14:15], s15, v164, v[62:63]
	v_mov_b32_e32 v5, v6
	v_mov_b32_e32 v13, v14
	v_mov_b32_e32 v21, v22
	v_mov_b32_e32 v29, v30
	v_mov_b32_e32 v37, v38
	v_mov_b32_e32 v45, v46
	v_mov_b32_e32 v53, v54
	v_mov_b32_e32 v61, v62
	v_lshl_add_u64 v[2:3], v[2:3], 2, s[2:3]
	v_lshlrev_b32_e32 v134, 2, v132
	v_lshl_add_u64 v[4:5], v[4:5], 2, s[2:3]
	v_lshl_add_u64 v[10:11], v[10:11], 2, s[2:3]
	v_lshl_add_u64 v[12:13], v[12:13], 2, s[2:3]
	v_lshl_add_u64 v[18:19], v[18:19], 2, s[2:3]
	v_lshl_add_u64 v[20:21], v[20:21], 2, s[2:3]
	v_lshl_add_u64 v[26:27], v[26:27], 2, s[2:3]
	v_lshl_add_u64 v[28:29], v[28:29], 2, s[2:3]
	v_lshl_add_u64 v[34:35], v[34:35], 2, s[2:3]
	v_lshl_add_u64 v[36:37], v[36:37], 2, s[2:3]
	v_lshl_add_u64 v[42:43], v[42:43], 2, s[2:3]
	v_lshl_add_u64 v[44:45], v[44:45], 2, s[2:3]
	v_lshl_add_u64 v[50:51], v[50:51], 2, s[2:3]
	v_lshl_add_u64 v[52:53], v[52:53], 2, s[2:3]
	v_lshl_add_u64 v[58:59], v[58:59], 2, s[2:3]
	v_lshl_add_u64 v[60:61], v[60:61], 2, s[2:3]
	v_lshl_add_u64 v[2:3], v[2:3], 0, v[134:135]
	v_lshl_add_u64 v[6:7], v[4:5], 0, v[134:135]
	v_lshl_add_u64 v[10:11], v[10:11], 0, v[134:135]
	v_lshl_add_u64 v[14:15], v[12:13], 0, v[134:135]
	v_lshl_add_u64 v[18:19], v[18:19], 0, v[134:135]
	v_lshl_add_u64 v[22:23], v[20:21], 0, v[134:135]
	v_lshl_add_u64 v[26:27], v[26:27], 0, v[134:135]
	v_lshl_add_u64 v[30:31], v[28:29], 0, v[134:135]
	v_lshl_add_u64 v[34:35], v[34:35], 0, v[134:135]
	v_lshl_add_u64 v[38:39], v[36:37], 0, v[134:135]
	v_lshl_add_u64 v[42:43], v[42:43], 0, v[134:135]
	v_lshl_add_u64 v[46:47], v[44:45], 0, v[134:135]
	v_lshl_add_u64 v[50:51], v[50:51], 0, v[134:135]
	v_lshl_add_u64 v[54:55], v[52:53], 0, v[134:135]
	v_lshl_add_u64 v[58:59], v[58:59], 0, v[134:135]
	v_lshl_add_u64 v[62:63], v[60:61], 0, v[134:135]
	global_load_dwordx4 v[2:5], v[2:3], off nt
	s_nop 0
	global_load_dwordx4 v[6:9], v[6:7], off nt
	s_nop 0
	global_load_dwordx4 v[10:13], v[10:11], off nt
	s_nop 0
	global_load_dwordx4 v[14:17], v[14:15], off nt
	s_nop 0
	global_load_dwordx4 v[18:21], v[18:19], off nt
	s_nop 0
	global_load_dwordx4 v[22:25], v[22:23], off nt
	s_nop 0
	global_load_dwordx4 v[26:29], v[26:27], off nt
	s_nop 0
	global_load_dwordx4 v[30:33], v[30:31], off nt
	s_nop 0
	global_load_dwordx4 v[34:37], v[34:35], off nt
	s_nop 0
	global_load_dwordx4 v[38:41], v[38:39], off nt
	s_nop 0
	global_load_dwordx4 v[42:45], v[42:43], off nt
	s_nop 0
	global_load_dwordx4 v[46:49], v[46:47], off nt
	s_nop 0
	global_load_dwordx4 v[50:53], v[50:51], off nt
	s_nop 0
	global_load_dwordx4 v[54:57], v[54:55], off nt
	s_nop 0
	global_load_dwordx4 v[58:61], v[58:59], off nt
	s_nop 0
	global_load_dwordx4 v[62:65], v[62:63], off nt
; #define GAS __attribute__((address_space(1)))
; #define LAS __attribute__((address_space(3)))
; #define LDS_WAIT() asm volatile("s_waitcnt lgkmcnt(0)" ::: "memory")
; __device__ __forceinline__ unsigned pk4_fp8(float a, float b, float c, float d) { int p = 0; p = __builtin_amdgcn_cvt_pk_fp8_f32(a, b, p, false); p = __builtin_amdgcn_cvt_pk_fp8_f32(c, d, p, true); return (unsigned)p; }
; __device__ __forceinline__ float clamp8s(float x) { return __builtin_amdgcn_fmed3f(x * W8_SCALE, -448.0f, 448.0f); }
; __device__ __forceinline__ void cv_finish(const CvItem& m, int lane, const f32x4 (&v)[16], LAS float* scr) {
;     const int rr = lane >> 3, c4 = (lane & 7) * 4;
; #pragma unroll
;     for (int i = 0; i < 16; ++i) *(LAS f32x4*)(scr + (8 * i + rr) * 36 + (c4 ^ (4 * ((i >> 1) & 7)))) = v[i];
;     LDS_WAIT(); asm volatile("" ::: "memory");
;     const int kc = lane & 7, nn = lane >> 3;
; #pragma unroll
;     for (int j = 0; j < 4; ++j) { const int n = nn + 8 * j; const LAS float* s = scr + (16 * kc) * 36 + (n ^ (4 * kc));
;         float x[16];
; #pragma unroll
;         for (int q = 0; q < 16; ++q) x[q] = s[q * 36];
;         if (m.f8) { v4u o;
;             o.x = pk4_fp8(clamp8s(x[0]), clamp8s(x[1]), clamp8s(x[2]), clamp8s(x[3])); o.y = pk4_fp8(clamp8s(x[4]), clamp8s(x[5]), clamp8s(x[6]), clamp8s(x[7]));
;             o.z = pk4_fp8(clamp8s(x[8]), clamp8s(x[9]), clamp8s(x[10]), clamp8s(x[11])); o.w = pk4_fp8(clamp8s(x[12]), clamp8s(x[13]), clamp8s(x[14]), clamp8s(x[15]));
;             __builtin_nontemporal_store(o, (GAS v4u*)((unsigned char*)m.dst + (size_t)n * m.ldt + 16 * kc)); }
; __device__ __forceinline__ void moe_pull(Frame& F, int k, int until) {
;     ...
;             if (f + t < NQ) cv_finish(ma, F.lane, va, scr);
.LBB0_1813:
	s_cmp_gt_i32 s54, 0x15cff
	v_add_u32_e32 v161, 0x400, v151
	v_add_u32_e32 v163, 0x600, v151
	s_cbranch_scc1 .LBB0_1827
	s_waitcnt vmcnt(31)
	ds_write_b128 v1, v[66:69]
	s_waitcnt vmcnt(30)
	ds_write_b128 v131, v[70:73]
	s_waitcnt vmcnt(29)
	ds_write_b128 v133, v[74:77]
	s_waitcnt vmcnt(28)
	ds_write_b128 v137, v[78:81]
	s_waitcnt vmcnt(27)
	ds_write_b128 v139, v[82:85] offset:4608
	s_waitcnt vmcnt(26)
	ds_write_b128 v139, v[86:89] offset:5760
	s_waitcnt vmcnt(25)
	ds_write_b128 v141, v[90:93] offset:6912
	s_waitcnt vmcnt(24)
	ds_write_b128 v141, v[94:97] offset:8064
	s_waitcnt vmcnt(23)
	ds_write_b128 v143, v[98:101] offset:9216
	s_waitcnt vmcnt(22)
	ds_write_b128 v143, v[102:105] offset:10368
	s_waitcnt vmcnt(21)
	ds_write_b128 v145, v[106:109] offset:11520
	s_waitcnt vmcnt(20)
	ds_write_b128 v145, v[110:113] offset:12672
	s_waitcnt vmcnt(19)
	ds_write_b128 v147, v[114:117] offset:13824
	s_waitcnt vmcnt(18)
	ds_write_b128 v147, v[118:121] offset:14976
	s_waitcnt vmcnt(17)
	ds_write_b128 v149, v[122:125] offset:16128
	s_waitcnt vmcnt(16)
	ds_write_b128 v149, v[126:129] offset:17280
	s_waitcnt lgkmcnt(0)
	ds_read2_b32 v[182:183], v151 offset1:36
	ds_read2_b32 v[180:181], v151 offset0:72 offset1:108
	ds_read2_b32 v[178:179], v151 offset0:144 offset1:180
	ds_read2_b32 v[176:177], v151 offset0:216 offset1:252
	ds_read2_b32 v[174:175], v161 offset0:32 offset1:68
	ds_read2_b32 v[172:173], v161 offset0:104 offset1:140
	ds_read2_b32 v[170:171], v161 offset0:176 offset1:212
	ds_read2_b32 v[168:169], v163 offset0:120 offset1:156
	s_cmp_lg_u32 s46, 0
	s_cselect_b64 s[14:15], -1, 0
	s_cmp_eq_u32 s46, 0
	s_cbranch_scc1 .LBB0_1860
	s_waitcnt lgkmcnt(7)
	v_mul_f32_e32 v134, 0x42800000, v182
	v_mul_f32_e32 v165, 0x42800000, v183
	v_med3_f32 v134, v134, s41, v159
	v_med3_f32 v165, v165, s41, v159
	v_mov_b32_e32 v184, v135
	v_cvt_pk_fp8_f32 v184, v134, v165
	s_waitcnt lgkmcnt(6)
	v_mul_f32_e32 v185, 0x42800000, v180
	v_mul_f32_e32 v165, 0x42800000, v181
	v_med3_f32 v134, v185, s41, v159
	v_med3_f32 v165, v165, s41, v159
	v_cvt_pk_fp8_f32 v184, v134, v165 op_sel:[0,0,1]
	s_waitcnt lgkmcnt(5)
	v_mul_f32_e32 v134, 0x42800000, v178
	v_mul_f32_e32 v165, 0x42800000, v179
	v_med3_f32 v134, v134, s41, v159
	v_med3_f32 v165, v165, s41, v159
	v_mov_b32_e32 v185, v135
	v_cvt_pk_fp8_f32 v185, v134, v165
	s_waitcnt lgkmcnt(4)
	v_mul_f32_e32 v186, 0x42800000, v176
	v_mul_f32_e32 v165, 0x42800000, v177
	v_med3_f32 v134, v186, s41, v159
	v_med3_f32 v165, v165, s41, v159
	v_cvt_pk_fp8_f32 v185, v134, v165 op_sel:[0,0,1]
	s_waitcnt lgkmcnt(3)
	v_mul_f32_e32 v134, 0x42800000, v174
	v_mul_f32_e32 v165, 0x42800000, v175
	v_med3_f32 v134, v134, s41, v159
	v_med3_f32 v165, v165, s41, v159
	v_mov_b32_e32 v186, v135
	v_cvt_pk_fp8_f32 v186, v134, v165
	s_waitcnt lgkmcnt(2)
	v_mul_f32_e32 v187, 0x42800000, v172
	v_mul_f32_e32 v165, 0x42800000, v173
	v_med3_f32 v134, v187, s41, v159
	v_med3_f32 v165, v165, s41, v159
	v_cvt_pk_fp8_f32 v186, v134, v165 op_sel:[0,0,1]
	s_waitcnt lgkmcnt(1)
	v_mul_f32_e32 v134, 0x42800000, v170
	v_mul_f32_e32 v165, 0x42800000, v171
	v_med3_f32 v134, v134, s41, v159
	v_med3_f32 v165, v165, s41, v159
	v_mov_b32_e32 v187, v135
	v_cvt_pk_fp8_f32 v187, v134, v165
	s_waitcnt lgkmcnt(0)
	v_mul_f32_e32 v188, 0x42800000, v168
	v_mul_f32_e32 v165, 0x42800000, v169
	v_med3_f32 v134, v188, s41, v159
	v_med3_f32 v165, v165, s41, v159
	v_cvt_pk_fp8_f32 v187, v134, v165 op_sel:[0,0,1]
	v_mov_b64_e32 v[188:189], s[10:11]
	v_mad_i64_i32 v[188:189], s[2:3], s45, v130, v[188:189]
	v_lshl_add_u64 v[188:189], v[188:189], 0, v[166:167]
	global_store_dwordx4 v[188:189], v[184:187], off nt
	s_cbranch_execnz .LBB0_1817

;     const int nb = N / 32, kb = sub / nb, nbi = sub % nb, k0 = kb * 128, n0 = nbi * 32;
;     const int dr = mode == 0 ? n0 : (256 * (n0 >> 7) + (n0 & 127) + (mode == 2 ? 128 : 0));
;     CvItem m; m.src = W + (size_t)k0 * N + n0; m.ldw = N; m.f8 = f8;
;     if (f8) { m.dst = (bf16*)((unsigned char*)WT + (size_t)dr * K + k0); m.ldt = K; } else { m.dst = WT + (size_t)dr * K + k0; m.ldt = K; }
;     return m;
; }
; __device__ __forceinline__ CvItem cv_item(Frame& F, int it) {
;     int r = it;
;     if (r < I_WIN0) return cv_make(F.in[7], DM, EIN, WSP(bf16, WS_WIN0), 0, r); r -= I_WIN0;
;     if (r < I_SQ) return cv_make(F.in[11], DM, DM, WSP(bf16, WS_WOUT0), 0, r); r -= I_SQ;
;     if (r < I_F) return cv_make(F.in[13], DM, DFF, WSP(bf16, WS_WGU0), 1, r, FFN8); r -= I_F;
;     if (r < I_F) return cv_make(F.in[14], DM, DFF, WSP(bf16, WS_WGU0), 2, r, FFN8); r -= I_F;
;     if (r < I_F) return cv_make(F.in[15], DFF, DM, WSP(bf16, WS_WD0), 0, r, FFN8); r -= I_F;
;     if (r < I_WIN1) return cv_make(F.in[19], DM, 2 * DM, WSP(bf16, WS_WIN1), 0, r); r -= I_WIN1;
;     if (r < I_SQ) return cv_make(F.in[27], DM, DM, WSP(bf16, WS_WOUT1), 0, r); r -= I_SQ;
;     if (r < 64 * I_G) { const int mtx = r >> 2, sub = r & 3, gt = mtx >> 5, zh = mtx & 31, z = zh >> 4, h = zh & 15;
;         return cv_make(F.in[gt ? 24 : 22] + (size_t)zh * 16384, 128, 128, WSP(bf16, WS_WGT) + (size_t)((z * 2 + gt) * 16 + h) * 16384, 0, sub); } r -= 64 * I_G;
;     const int w = r / (8 * I_ME), rr = r % (8 * I_ME), e = rr / I_ME, sub = rr % I_ME;
;     if (w == 0) return cv_make(F.in[31] + (size_t)e * DM * DFFE, DM, DFFE, (bf16*)(F.ws + WS_MWGU + (size_t)e * 2 * DFFE * DM), 1, sub, 1);
;     if (w == 1) return cv_make(F.in[32] + (size_t)e * DM * DFFE, DM, DFFE, (bf16*)(F.ws + WS_MWGU + (size_t)e * 2 * DFFE * DM), 2, sub, 1);
;     return cv_make(F.in[33] + (size_t)e * DFFE * DM, DFFE, DM, (bf16*)(F.ws + WS_MWD + (size_t)e * DM * DFFE), 0, sub, 1);
; __device__ __forceinline__ void moe_pull(Frame& F, int k, int until) {
;     ...
;             if (t + 2 < 8 && f + t + 2 < NQ) { ma = cv_item(F, NEARLY + f + t + 2); cv_load(ma, F.lane, va); }
.LBB0_1827:
	s_cmp_gt_u32 s51, 5
	s_cselect_b64 s[14:15], -1, 0
	s_cmp_gt_i32 s54, 0x15cfd
	s_cselect_b64 s[2:3], -1, 0
	s_or_b64 s[2:3], s[14:15], s[2:3]
	s_and_b64 vcc, exec, s[2:3]
	s_cbranch_vccz .Lcv15_go1
	s_waitcnt vmcnt(0)
	s_branch .LBB0_1848
.Lcv15_go1:
	s_add_i32 s4, s54, 0x2e00
	s_cmpk_gt_u32 s4, 0x35fd
	s_mov_b64 s[18:19], -1
	s_cbranch_scc0 .LBB0_1845
	s_cmpk_gt_u32 s4, 0x39fd
	s_cbranch_scc0 .LBB0_1842
	s_cmpk_gt_u32 s4, 0x3afd
	s_cbranch_scc0 .LBB0_1839
	s_lshr_b32 s2, s53, 12
	s_mul_hi_u32 s2, s2, 0x24924925
	s_mulk_i32 s2, 0x7000
	s_sub_i32 s2, s47, s2
	s_add_i32 s2, s51, s2
	s_bfe_u32 s4, s2, 0x70009
	s_mulk_i32 s4, 0x2493
	s_lshr_b32 s46, s4, 16
	s_mul_i32 s4, s46, 0xe00
	s_add_i32 s3, s54, 0xfffff302
	s_sub_i32 s4, s2, s4
	s_cmpk_gt_u32 s3, 0x6fff
	s_mul_i32 s55, s46, 0x3800000
	s_cbranch_scc0 .LBB0_1836
	s_add_i32 s2, s54, 0xffff8302
	s_cmpk_gt_u32 s2, 0x6fff
	s_mov_b64 s[16:17], -1
	s_cbranch_scc0 .LBB0_1834
	v_readlane_b32 s56, v250, 0
	v_readlane_b32 s58, v250, 2
	v_readlane_b32 s59, v250, 3
	s_add_u32 s2, s58, s55
	s_addc_u32 s3, s59, 0
	s_mul_i32 s10, s46, 0xe00000
	s_add_u32 s10, s21, s10
	s_addc_u32 s11, s22, 0
	s_lshl_b32 s17, s4, 5
	s_lshl_b32 s16, s4, 1
	s_and_b32 s17, s17, 0x7e0
	s_and_b32 s16, s16, 0x1f80
	s_mul_i32 s18, s17, 0x1c00
	s_add_u32 s10, s10, s18
	s_addc_u32 s11, s11, 0
	s_add_u32 s10, s10, s16
	s_addc_u32 s11, s11, 0
	s_lshl_b32 s16, s16, 13
	s_add_u32 s2, s2, s16
	s_addc_u32 s3, s3, 0
	s_lshl_b32 s16, s17, 2
	s_add_u32 s2, s2, s16
	v_readlane_b32 s57, v250, 1
	v_readlane_b32 s60, v250, 4
	v_readlane_b32 s61, v250, 5
	v_readlane_b32 s62, v250, 6
	v_readlane_b32 s63, v250, 7
	s_addc_u32 s3, s3, 0
	s_mov_b64 s[16:17], 0

; #define GAS __attribute__((address_space(1)))
; __device__ __forceinline__ void cv_load(const CvItem& m, int lane, f32x4 (&v)[16]) {
;     const int rr = lane >> 3, c4 = (lane & 7) * 4;
; #pragma unroll
;     for (int i = 0; i < 16; ++i) v[i] = __builtin_nontemporal_load((const GAS f32x4*)(m.src + (size_t)(8 * i + rr) * m.ldw + c4));
; }
.LBB0_1847:
	v_mad_u64_u32 v[66:67], s[18:19], s16, v130, 0
	v_mad_u64_u32 v[74:75], s[18:19], s16, v138, 0
	v_mad_u64_u32 v[82:83], s[18:19], s16, v142, 0
	v_mad_u64_u32 v[90:91], s[18:19], s16, v146, 0
	v_mad_u64_u32 v[98:99], s[18:19], s16, v150, 0
	v_mad_u64_u32 v[106:107], s[18:19], s16, v154, 0
	v_mad_u64_u32 v[114:115], s[18:19], s16, v158, 0
	v_mad_u64_u32 v[122:123], s[18:19], s16, v162, 0
	v_mov_b32_e32 v68, v67
	v_mov_b32_e32 v76, v75
	v_mov_b32_e32 v84, v83
	v_mov_b32_e32 v92, v91
	v_mov_b32_e32 v100, v99
	v_mov_b32_e32 v108, v107
	v_mov_b32_e32 v116, v115
	v_mov_b32_e32 v124, v123
	v_mad_u64_u32 v[68:69], s[18:19], s17, v130, v[68:69]
	v_mad_u64_u32 v[76:77], s[18:19], s17, v138, v[76:77]
	v_mad_u64_u32 v[84:85], s[18:19], s17, v142, v[84:85]
	v_mad_u64_u32 v[92:93], s[18:19], s17, v146, v[92:93]
	v_mad_u64_u32 v[100:101], s[18:19], s17, v150, v[100:101]
	v_mad_u64_u32 v[108:109], s[18:19], s17, v154, v[108:109]
	v_mad_u64_u32 v[116:117], s[18:19], s17, v158, v[116:117]
	v_mad_u64_u32 v[124:125], s[18:19], s17, v162, v[124:125]
	v_mov_b32_e32 v67, v68
	v_mad_u64_u32 v[68:69], s[18:19], s16, v136, 0
	v_mov_b32_e32 v75, v76
	v_mad_u64_u32 v[76:77], s[18:19], s16, v140, 0
	v_mov_b32_e32 v83, v84
	v_mad_u64_u32 v[84:85], s[18:19], s16, v144, 0
	v_mov_b32_e32 v91, v92
	v_mad_u64_u32 v[92:93], s[18:19], s16, v148, 0
	v_mov_b32_e32 v99, v100
	v_mad_u64_u32 v[100:101], s[18:19], s16, v152, 0
	v_mov_b32_e32 v107, v108
	v_mad_u64_u32 v[108:109], s[18:19], s16, v156, 0
	v_mov_b32_e32 v115, v116
	v_mad_u64_u32 v[116:117], s[18:19], s16, v160, 0
	v_mov_b32_e32 v123, v124
	v_mad_u64_u32 v[124:125], s[18:19], s16, v164, 0
	v_mov_b32_e32 v70, v69
	v_mov_b32_e32 v78, v77
	v_mov_b32_e32 v86, v85
	v_mov_b32_e32 v94, v93
	v_mov_b32_e32 v102, v101
	v_mov_b32_e32 v110, v109
	v_mov_b32_e32 v118, v117
	v_mov_b32_e32 v126, v125
	v_mad_u64_u32 v[70:71], s[18:19], s17, v136, v[70:71]
	v_mad_u64_u32 v[78:79], s[18:19], s17, v140, v[78:79]
	v_mad_u64_u32 v[86:87], s[18:19], s17, v144, v[86:87]
	v_mad_u64_u32 v[94:95], s[18:19], s17, v148, v[94:95]
	v_mad_u64_u32 v[102:103], s[18:19], s17, v152, v[102:103]
	v_mad_u64_u32 v[110:111], s[18:19], s17, v156, v[110:111]
	v_mad_u64_u32 v[118:119], s[18:19], s17, v160, v[118:119]
	v_mad_u64_u32 v[126:127], s[16:17], s17, v164, v[126:127]
	v_mov_b32_e32 v69, v70
	v_mov_b32_e32 v77, v78
	v_mov_b32_e32 v85, v86
	v_mov_b32_e32 v93, v94
	v_mov_b32_e32 v101, v102
	v_mov_b32_e32 v109, v110
	v_mov_b32_e32 v117, v118
	v_mov_b32_e32 v125, v126
	v_lshl_add_u64 v[66:67], v[66:67], 2, s[2:3]
	v_lshlrev_b32_e32 v134, 2, v132
	v_lshl_add_u64 v[68:69], v[68:69], 2, s[2:3]
	v_lshl_add_u64 v[74:75], v[74:75], 2, s[2:3]
	v_lshl_add_u64 v[76:77], v[76:77], 2, s[2:3]
	v_lshl_add_u64 v[82:83], v[82:83], 2, s[2:3]
	v_lshl_add_u64 v[84:85], v[84:85], 2, s[2:3]
	v_lshl_add_u64 v[90:91], v[90:91], 2, s[2:3]
	v_lshl_add_u64 v[92:93], v[92:93], 2, s[2:3]
	v_lshl_add_u64 v[98:99], v[98:99], 2, s[2:3]
	v_lshl_add_u64 v[100:101], v[100:101], 2, s[2:3]
	v_lshl_add_u64 v[106:107], v[106:107], 2, s[2:3]
	v_lshl_add_u64 v[108:109], v[108:109], 2, s[2:3]
	v_lshl_add_u64 v[114:115], v[114:115], 2, s[2:3]
	v_lshl_add_u64 v[116:117], v[116:117], 2, s[2:3]
	v_lshl_add_u64 v[122:123], v[122:123], 2, s[2:3]
	v_lshl_add_u64 v[124:125], v[124:125], 2, s[2:3]
	v_lshl_add_u64 v[66:67], v[66:67], 0, v[134:135]
	v_lshl_add_u64 v[70:71], v[68:69], 0, v[134:135]
	v_lshl_add_u64 v[74:75], v[74:75], 0, v[134:135]
	v_lshl_add_u64 v[78:79], v[76:77], 0, v[134:135]
	v_lshl_add_u64 v[82:83], v[82:83], 0, v[134:135]
	v_lshl_add_u64 v[86:87], v[84:85], 0, v[134:135]
	v_lshl_add_u64 v[90:91], v[90:91], 0, v[134:135]
	v_lshl_add_u64 v[94:95], v[92:93], 0, v[134:135]
	v_lshl_add_u64 v[98:99], v[98:99], 0, v[134:135]
	v_lshl_add_u64 v[102:103], v[100:101], 0, v[134:135]
	v_lshl_add_u64 v[106:107], v[106:107], 0, v[134:135]
	v_lshl_add_u64 v[110:111], v[108:109], 0, v[134:135]
	v_lshl_add_u64 v[114:115], v[114:115], 0, v[134:135]
	v_lshl_add_u64 v[118:119], v[116:117], 0, v[134:135]
	v_lshl_add_u64 v[122:123], v[122:123], 0, v[134:135]
	v_lshl_add_u64 v[126:127], v[124:125], 0, v[134:135]
	global_load_dwordx4 v[66:69], v[66:67], off nt
	s_nop 0
	global_load_dwordx4 v[70:73], v[70:71], off nt
	s_nop 0
	global_load_dwordx4 v[74:77], v[74:75], off nt
	s_nop 0
	global_load_dwordx4 v[78:81], v[78:79], off nt
	s_nop 0
	global_load_dwordx4 v[82:85], v[82:83], off nt
	s_nop 0
	global_load_dwordx4 v[86:89], v[86:87], off nt
	s_nop 0
	global_load_dwordx4 v[90:93], v[90:91], off nt
	s_nop 0
	global_load_dwordx4 v[94:97], v[94:95], off nt
	s_nop 0
	global_load_dwordx4 v[98:101], v[98:99], off nt
	s_nop 0
	global_load_dwordx4 v[102:105], v[102:103], off nt
	s_nop 0
	global_load_dwordx4 v[106:109], v[106:107], off nt
	s_nop 0
	global_load_dwordx4 v[110:113], v[110:111], off nt
	s_nop 0
	global_load_dwordx4 v[114:117], v[114:115], off nt
	s_nop 0
	global_load_dwordx4 v[118:121], v[118:119], off nt
	s_nop 0
	global_load_dwordx4 v[122:125], v[122:123], off nt
	s_nop 0
	global_load_dwordx4 v[126:129], v[126:127], off nt
; #define GAS __attribute__((address_space(1)))
; #define LAS __attribute__((address_space(3)))
; #define LDS_WAIT() asm volatile("s_waitcnt lgkmcnt(0)" ::: "memory")
; __device__ __forceinline__ unsigned pk4_fp8(float a, float b, float c, float d) { int p = 0; p = __builtin_amdgcn_cvt_pk_fp8_f32(a, b, p, false); p = __builtin_amdgcn_cvt_pk_fp8_f32(c, d, p, true); return (unsigned)p; }
; __device__ __forceinline__ float clamp8s(float x) { return __builtin_amdgcn_fmed3f(x * W8_SCALE, -448.0f, 448.0f); }
; __device__ __forceinline__ void cv_finish(const CvItem& m, int lane, const f32x4 (&v)[16], LAS float* scr) {
;     const int rr = lane >> 3, c4 = (lane & 7) * 4;
; #pragma unroll
;     for (int i = 0; i < 16; ++i) *(LAS f32x4*)(scr + (8 * i + rr) * 36 + (c4 ^ (4 * ((i >> 1) & 7)))) = v[i];
;     LDS_WAIT(); asm volatile("" ::: "memory");
;     const int kc = lane & 7, nn = lane >> 3;
; #pragma unroll
;     for (int j = 0; j < 4; ++j) { const int n = nn + 8 * j; const LAS float* s = scr + (16 * kc) * 36 + (n ^ (4 * kc));
;         float x[16];
; #pragma unroll
;         for (int q = 0; q < 16; ++q) x[q] = s[q * 36];
;         if (m.f8) { v4u o;
;             o.x = pk4_fp8(clamp8s(x[0]), clamp8s(x[1]), clamp8s(x[2]), clamp8s(x[3])); o.y = pk4_fp8(clamp8s(x[4]), clamp8s(x[5]), clamp8s(x[6]), clamp8s(x[7]));
;             o.z = pk4_fp8(clamp8s(x[8]), clamp8s(x[9]), clamp8s(x[10]), clamp8s(x[11])); o.w = pk4_fp8(clamp8s(x[12]), clamp8s(x[13]), clamp8s(x[14]), clamp8s(x[15]));
;             __builtin_nontemporal_store(o, (GAS v4u*)((unsigned char*)m.dst + (size_t)n * m.ldt + 16 * kc)); }
; __device__ __forceinline__ void moe_pull(Frame& F, int k, int until) {
;     ...
;             if (f + t + 1 < NQ) cv_finish(mb, F.lane, vb, scr);
.LBB0_1848:
	s_andn2_b64 vcc, exec, s[12:13]
	s_cbranch_vccnz .LBB0_1787
	s_waitcnt vmcnt(31)
	ds_write_b128 v1, v[2:5]
	s_waitcnt vmcnt(30)
	ds_write_b128 v131, v[6:9]
	s_waitcnt vmcnt(29)
	ds_write_b128 v133, v[10:13]
	s_waitcnt vmcnt(28)
	ds_write_b128 v137, v[14:17]
	s_waitcnt vmcnt(27)
	ds_write_b128 v139, v[18:21] offset:4608
	s_waitcnt vmcnt(26)
	ds_write_b128 v139, v[22:25] offset:5760
	s_waitcnt vmcnt(25)
	ds_write_b128 v141, v[26:29] offset:6912
	s_waitcnt vmcnt(24)
	ds_write_b128 v141, v[30:33] offset:8064
	s_waitcnt vmcnt(23)
	ds_write_b128 v143, v[34:37] offset:9216
	s_waitcnt vmcnt(22)
	ds_write_b128 v143, v[38:41] offset:10368
	s_waitcnt vmcnt(21)
	ds_write_b128 v145, v[42:45] offset:11520
	s_waitcnt vmcnt(20)
	ds_write_b128 v145, v[46:49] offset:12672
	s_waitcnt vmcnt(19)
	ds_write_b128 v147, v[50:53] offset:13824
	s_waitcnt vmcnt(18)
	ds_write_b128 v147, v[54:57] offset:14976
	s_waitcnt vmcnt(17)
	ds_write_b128 v149, v[58:61] offset:16128
	s_waitcnt vmcnt(16)
	ds_write_b128 v149, v[62:65] offset:17280
	s_waitcnt lgkmcnt(0)
	s_waitcnt lgkmcnt(14)
	ds_read2_b32 v[182:183], v151 offset1:36
	ds_read2_b32 v[180:181], v151 offset0:72 offset1:108
	ds_read2_b32 v[178:179], v151 offset0:144 offset1:180
	ds_read2_b32 v[176:177], v151 offset0:216 offset1:252
	ds_read2_b32 v[174:175], v161 offset0:32 offset1:68
	ds_read2_b32 v[172:173], v161 offset0:104 offset1:140
	ds_read2_b32 v[170:171], v161 offset0:176 offset1:212
	ds_read2_b32 v[168:169], v163 offset0:120 offset1:156
	s_cmp_lg_u32 s44, 0
	s_cselect_b64 s[12:13], -1, 0
	s_cmp_eq_u32 s44, 0
	s_cbranch_scc1 .LBB0_1864
	s_waitcnt lgkmcnt(7)
	v_mul_f32_e32 v134, 0x42800000, v182
	v_mul_f32_e32 v161, 0x42800000, v183
	v_med3_f32 v134, v134, s41, v159
	v_med3_f32 v161, v161, s41, v159
	v_mov_b32_e32 v184, v135
	v_cvt_pk_fp8_f32 v184, v134, v161
	s_waitcnt lgkmcnt(6)
	v_mul_f32_e32 v163, 0x42800000, v180
	v_mul_f32_e32 v161, 0x42800000, v181
	v_med3_f32 v134, v163, s41, v159
	v_med3_f32 v161, v161, s41, v159
	v_cvt_pk_fp8_f32 v184, v134, v161 op_sel:[0,0,1]
	s_waitcnt lgkmcnt(5)
	v_mul_f32_e32 v134, 0x42800000, v178
	v_mul_f32_e32 v161, 0x42800000, v179
	v_med3_f32 v134, v134, s41, v159
	v_med3_f32 v161, v161, s41, v159
	v_mov_b32_e32 v185, v135
	v_cvt_pk_fp8_f32 v185, v134, v161
	s_waitcnt lgkmcnt(4)
	v_mul_f32_e32 v163, 0x42800000, v176
	v_mul_f32_e32 v161, 0x42800000, v177
	v_med3_f32 v134, v163, s41, v159
	v_med3_f32 v161, v161, s41, v159
	v_cvt_pk_fp8_f32 v185, v134, v161 op_sel:[0,0,1]
	s_waitcnt lgkmcnt(3)
	v_mul_f32_e32 v134, 0x42800000, v174
	v_mul_f32_e32 v161, 0x42800000, v175
	v_med3_f32 v134, v134, s41, v159
	v_med3_f32 v161, v161, s41, v159
	v_mov_b32_e32 v186, v135
	v_cvt_pk_fp8_f32 v186, v134, v161
	s_waitcnt lgkmcnt(2)
	v_mul_f32_e32 v163, 0x42800000, v172
	v_mul_f32_e32 v161, 0x42800000, v173
	v_med3_f32 v134, v163, s41, v159
	v_med3_f32 v161, v161, s41, v159
	v_cvt_pk_fp8_f32 v186, v134, v161 op_sel:[0,0,1]
	s_waitcnt lgkmcnt(1)
	v_mul_f32_e32 v134, 0x42800000, v170
	v_mul_f32_e32 v161, 0x42800000, v171
	v_med3_f32 v134, v134, s41, v159
	v_med3_f32 v161, v161, s41, v159
	v_mov_b32_e32 v187, v135
	v_cvt_pk_fp8_f32 v187, v134, v161
	s_waitcnt lgkmcnt(0)
	v_mul_f32_e32 v163, 0x42800000, v168
	v_mul_f32_e32 v161, 0x42800000, v169
	v_med3_f32 v134, v163, s41, v159
	v_med3_f32 v161, v161, s41, v159
	v_cvt_pk_fp8_f32 v187, v134, v161 op_sel:[0,0,1]
	v_mov_b64_e32 v[188:189], s[8:9]
	v_mad_i64_i32 v[188:189], s[2:3], s42, v130, v[188:189]
	v_lshl_add_u64 v[188:189], v[188:189], 0, v[166:167]
	global_store_dwordx4 v[188:189], v[184:187], off nt
	v_lshlrev_b32_e32 v134, 1, v166
	s_cbranch_execnz .LBB0_1852
